# parallel adaLN mods (192 WGs x 8 row slices, LDS reduce), unrolled silu table, phase-1 reorder modulate_rows before fold GEMM
# speedup vs baseline: 1.0125x; 1.0125x over previous
.LBB0_15:
	s_lshr_b32 s86, s6, 6
	s_cmp_lt_i32 s90, 1
	s_cselect_b64 s[12:13], -1, 0
	s_cmp_gt_i32 s91, 0
	s_cselect_b64 s[0:1], -1, 0
	s_and_b64 s[0:1], s[12:13], s[0:1]
	s_andn2_b64 vcc, exec, s[0:1]
	v_mbcnt_lo_u32_b32 v132, -1, 0
	s_cbranch_vccnz .LBB0_130
	s_mov_b64 s[18:19], s[84:85]
	s_mov_b32 s0, s86
	v_mbcnt_hi_u32_b32 v1, -1, v132
	s_nop 0
	v_lshl_add_u32 v8, s0, 6, v1
	s_load_dwordx2 s[16:17], s[18:19], 0x100
	s_load_dwordx2 s[8:9], s[18:19], 0x8
	s_load_dwordx2 s[4:5], s[18:19], 0x18
	v_readfirstlane_b32 s10, v8
	v_lshlrev_b32_e32 v1, 2, v8
	s_waitcnt lgkmcnt(0)
	global_load_dword v194, v1, s[8:9]
	global_load_dword v195, v1, s[8:9] offset:2048
	s_add_u32 s8, s8, 0x1000
	s_addc_u32 s9, s9, 0
	global_load_dword v196, v1, s[8:9]
	global_load_dword v197, v1, s[8:9] offset:2048
	s_add_u32 s8, s8, 0x1000
	s_addc_u32 s9, s9, 0
	global_load_dword v198, v1, s[8:9]
	global_load_dword v199, v1, s[8:9] offset:2048
	s_add_u32 s8, s8, 0x1000
	s_addc_u32 s9, s9, 0
	global_load_dword v200, v1, s[8:9]
	global_load_dword v201, v1, s[8:9] offset:2048
	s_add_u32 s8, s8, 0x1000
	s_addc_u32 s9, s9, 0
	global_load_dword v202, v1, s[8:9]
	global_load_dword v203, v1, s[8:9] offset:2048
	s_add_u32 s8, s8, 0x1000
	s_addc_u32 s9, s9, 0
	global_load_dword v204, v1, s[8:9]
	global_load_dword v205, v1, s[8:9] offset:2048
	s_add_u32 s8, s8, 0x1000
	s_addc_u32 s9, s9, 0
	global_load_dword v206, v1, s[8:9]
	global_load_dword v207, v1, s[8:9] offset:2048
	s_add_u32 s8, s8, 0x1000
	s_addc_u32 s9, s9, 0
	global_load_dword v208, v1, s[8:9]
	global_load_dword v209, v1, s[8:9] offset:2048
	global_load_dword v210, v1, s[4:5]
	global_load_dword v211, v1, s[4:5] offset:2048
	s_waitcnt vmcnt(16)
	v_mul_f32_e32 v2, 0xbfb8aa3b, v194
	v_mul_f32_e32 v3, 0xbfb8aa3b, v195
	v_exp_f32_e32 v2, v2
	v_exp_f32_e32 v3, v3
	s_nop 0
	v_add_f32_e32 v2, 1.0, v2
	v_add_f32_e32 v3, 1.0, v3
	v_rcp_f32_e32 v2, v2
	v_rcp_f32_e32 v3, v3
	s_nop 0
	v_mul_f32_e32 v2, v194, v2
	v_mul_f32_e32 v3, v195, v3
	ds_write_b32 v1, v2
	ds_write_b32 v1, v3 offset:2048
	s_waitcnt vmcnt(14)
	v_mul_f32_e32 v2, 0xbfb8aa3b, v196
	v_mul_f32_e32 v3, 0xbfb8aa3b, v197
	v_exp_f32_e32 v2, v2
	v_exp_f32_e32 v3, v3
	s_nop 0
	v_add_f32_e32 v2, 1.0, v2
	v_add_f32_e32 v3, 1.0, v3
	v_rcp_f32_e32 v2, v2
	v_rcp_f32_e32 v3, v3
	s_nop 0
	v_mul_f32_e32 v2, v196, v2
	v_mul_f32_e32 v3, v197, v3
	ds_write_b32 v1, v2 offset:4096
	ds_write_b32 v1, v3 offset:6144
	s_waitcnt vmcnt(12)
	v_mul_f32_e32 v2, 0xbfb8aa3b, v198
	v_mul_f32_e32 v3, 0xbfb8aa3b, v199
	v_exp_f32_e32 v2, v2
	v_exp_f32_e32 v3, v3
	s_nop 0
	v_add_f32_e32 v2, 1.0, v2
	v_add_f32_e32 v3, 1.0, v3
	v_rcp_f32_e32 v2, v2
	v_rcp_f32_e32 v3, v3
	s_nop 0
	v_mul_f32_e32 v2, v198, v2
	v_mul_f32_e32 v3, v199, v3
	ds_write_b32 v1, v2 offset:8192
	ds_write_b32 v1, v3 offset:10240
	s_waitcnt vmcnt(10)
	v_mul_f32_e32 v2, 0xbfb8aa3b, v200
	v_mul_f32_e32 v3, 0xbfb8aa3b, v201
	v_exp_f32_e32 v2, v2
	v_exp_f32_e32 v3, v3
	s_nop 0
	v_add_f32_e32 v2, 1.0, v2
	v_add_f32_e32 v3, 1.0, v3
	v_rcp_f32_e32 v2, v2
	v_rcp_f32_e32 v3, v3
	s_nop 0
	v_mul_f32_e32 v2, v200, v2
	v_mul_f32_e32 v3, v201, v3
	ds_write_b32 v1, v2 offset:12288
	ds_write_b32 v1, v3 offset:14336
	s_waitcnt vmcnt(8)
	v_mul_f32_e32 v2, 0xbfb8aa3b, v202
	v_mul_f32_e32 v3, 0xbfb8aa3b, v203
	v_exp_f32_e32 v2, v2
	v_exp_f32_e32 v3, v3
	s_nop 0
	v_add_f32_e32 v2, 1.0, v2
	v_add_f32_e32 v3, 1.0, v3
	v_rcp_f32_e32 v2, v2
	v_rcp_f32_e32 v3, v3
	s_nop 0
	v_mul_f32_e32 v2, v202, v2
	v_mul_f32_e32 v3, v203, v3
	ds_write_b32 v1, v2 offset:16384
	ds_write_b32 v1, v3 offset:18432
	s_waitcnt vmcnt(6)
	v_mul_f32_e32 v2, 0xbfb8aa3b, v204
	v_mul_f32_e32 v3, 0xbfb8aa3b, v205
	v_exp_f32_e32 v2, v2
	v_exp_f32_e32 v3, v3
	s_nop 0
	v_add_f32_e32 v2, 1.0, v2
	v_add_f32_e32 v3, 1.0, v3
	v_rcp_f32_e32 v2, v2
	v_rcp_f32_e32 v3, v3
	s_nop 0
	v_mul_f32_e32 v2, v204, v2
	v_mul_f32_e32 v3, v205, v3
	ds_write_b32 v1, v2 offset:20480
	ds_write_b32 v1, v3 offset:22528
	s_waitcnt vmcnt(4)
	v_mul_f32_e32 v2, 0xbfb8aa3b, v206
	v_mul_f32_e32 v3, 0xbfb8aa3b, v207
	v_exp_f32_e32 v2, v2
	v_exp_f32_e32 v3, v3
	s_nop 0
	v_add_f32_e32 v2, 1.0, v2
	v_add_f32_e32 v3, 1.0, v3
	v_rcp_f32_e32 v2, v2
	v_rcp_f32_e32 v3, v3
	s_nop 0
	v_mul_f32_e32 v2, v206, v2
	v_mul_f32_e32 v3, v207, v3
	ds_write_b32 v1, v2 offset:24576
	ds_write_b32 v1, v3 offset:26624
	s_waitcnt vmcnt(2)
	v_mul_f32_e32 v2, 0xbfb8aa3b, v208
	v_mul_f32_e32 v3, 0xbfb8aa3b, v209
	v_exp_f32_e32 v2, v2
	v_exp_f32_e32 v3, v3
	s_nop 0
	v_add_f32_e32 v2, 1.0, v2
	v_add_f32_e32 v3, 1.0, v3
	v_rcp_f32_e32 v2, v2
	v_rcp_f32_e32 v3, v3
	s_nop 0
	v_mul_f32_e32 v2, v208, v2
	v_mul_f32_e32 v3, v209, v3
	ds_write_b32 v1, v2 offset:28672
	ds_write_b32 v1, v3 offset:30720
	s_waitcnt vmcnt(0)
	v_mul_f32_e32 v2, 0xbfb8aa3b, v210
	v_mul_f32_e32 v3, 0xbfb8aa3b, v211
	v_exp_f32_e32 v2, v2
	v_exp_f32_e32 v3, v3
	s_nop 0
	v_add_f32_e32 v2, 1.0, v2
	v_add_f32_e32 v3, 1.0, v3
	v_rcp_f32_e32 v2, v2
	v_rcp_f32_e32 v3, v3
	s_nop 0
	v_mul_f32_e32 v2, v210, v2
	v_mul_f32_e32 v3, v211, v3
	ds_write_b32 v1, v2 offset:32768
	ds_write_b32 v1, v3 offset:34816
	s_lshl_b32 s0, s82, 3
	s_ashr_i32 s43, s10, 6
	s_add_i32 s41, s43, s0
	v_and_b32_e32 v22, 63, v8
	s_cmpk_lt_i32 s82, 0xc0
	s_waitcnt lgkmcnt(0)
	s_barrier
	s_cbranch_scc0 .LBB0_23
	s_cmpk_ge_i32 s82, 0x60
	s_cselect_b32 s4, 1, 0
	s_mul_i32 s0, s4, 0x60
	s_sub_i32 s5, s82, s0
	s_load_dwordx2 s[0:1], s[18:19], 0x20
	s_load_dwordx2 s[6:7], s[18:19], 0x28
	v_lshl_or_b32 v12, s5, 6, v22
	v_lshlrev_b32_e32 v13, 2, v12
	s_mul_i32 s8, s4, 0x1800000
	s_mul_i32 s9, s43, 0x300000
	s_add_u32 s8, s8, s9
	s_mul_i32 s9, s4, 0x6000
	s_lshl_b32 s11, s43, 9
	v_mov_b32_e32 v14, s11
	s_waitcnt lgkmcnt(0)
	s_add_u32 s0, s0, s8
	s_addc_u32 s1, s1, 0
	s_add_u32 s6, s6, s9
	s_addc_u32 s7, s7, 0
	global_load_dword v21, v13, s[6:7]
	v_mov_b32_e32 v2, 0
	v_mov_b32_e32 v3, 0
	v_mov_b32_e32 v4, 0
	v_mov_b32_e32 v5, 0
	v_mov_b32_e32 v6, 0
	v_mov_b32_e32 v7, 0
	v_mov_b32_e32 v9, 0
	v_mov_b32_e32 v10, 0
	v_mov_b32_e32 v11, 0
	global_load_dword v194, v13, s[0:1]
	s_add_u32 s0, s0, 0x6000
	s_addc_u32 s1, s1, 0
	global_load_dword v195, v13, s[0:1]
	s_add_u32 s0, s0, 0x6000
	s_addc_u32 s1, s1, 0
	global_load_dword v196, v13, s[0:1]
	s_add_u32 s0, s0, 0x6000
	s_addc_u32 s1, s1, 0
	global_load_dword v197, v13, s[0:1]
	s_add_u32 s0, s0, 0x6000
	s_addc_u32 s1, s1, 0
	global_load_dword v198, v13, s[0:1]
	s_add_u32 s0, s0, 0x6000
	s_addc_u32 s1, s1, 0
	global_load_dword v199, v13, s[0:1]
	s_add_u32 s0, s0, 0x6000
	s_addc_u32 s1, s1, 0
	global_load_dword v200, v13, s[0:1]
	s_add_u32 s0, s0, 0x6000
	s_addc_u32 s1, s1, 0
	global_load_dword v201, v13, s[0:1]
	s_add_u32 s0, s0, 0x6000
	s_addc_u32 s1, s1, 0
	global_load_dword v202, v13, s[0:1]
	s_add_u32 s0, s0, 0x6000
	s_addc_u32 s1, s1, 0
	global_load_dword v203, v13, s[0:1]
	s_add_u32 s0, s0, 0x6000
	s_addc_u32 s1, s1, 0
	global_load_dword v204, v13, s[0:1]
	s_add_u32 s0, s0, 0x6000
	s_addc_u32 s1, s1, 0
	global_load_dword v205, v13, s[0:1]
	s_add_u32 s0, s0, 0x6000
	s_addc_u32 s1, s1, 0
	global_load_dword v206, v13, s[0:1]
	s_add_u32 s0, s0, 0x6000
	s_addc_u32 s1, s1, 0
	global_load_dword v207, v13, s[0:1]
	s_add_u32 s0, s0, 0x6000
	s_addc_u32 s1, s1, 0
	global_load_dword v208, v13, s[0:1]
	s_add_u32 s0, s0, 0x6000
	s_addc_u32 s1, s1, 0
	global_load_dword v209, v13, s[0:1]
	s_add_u32 s0, s0, 0x6000
	s_addc_u32 s1, s1, 0
	global_load_dword v210, v13, s[0:1]
	s_add_u32 s0, s0, 0x6000
	s_addc_u32 s1, s1, 0
	global_load_dword v211, v13, s[0:1]
	s_add_u32 s0, s0, 0x6000
	s_addc_u32 s1, s1, 0
	global_load_dword v212, v13, s[0:1]
	s_add_u32 s0, s0, 0x6000
	s_addc_u32 s1, s1, 0
	global_load_dword v213, v13, s[0:1]
	s_add_u32 s0, s0, 0x6000
	s_addc_u32 s1, s1, 0
	global_load_dword v214, v13, s[0:1]
	s_add_u32 s0, s0, 0x6000
	s_addc_u32 s1, s1, 0
	global_load_dword v215, v13, s[0:1]
	s_add_u32 s0, s0, 0x6000
	s_addc_u32 s1, s1, 0
	global_load_dword v216, v13, s[0:1]
	s_add_u32 s0, s0, 0x6000
	s_addc_u32 s1, s1, 0
	global_load_dword v217, v13, s[0:1]
	s_add_u32 s0, s0, 0x6000
	s_addc_u32 s1, s1, 0
	global_load_dword v218, v13, s[0:1]
	s_add_u32 s0, s0, 0x6000
	s_addc_u32 s1, s1, 0
	global_load_dword v219, v13, s[0:1]
	s_add_u32 s0, s0, 0x6000
	s_addc_u32 s1, s1, 0
	global_load_dword v220, v13, s[0:1]
	s_add_u32 s0, s0, 0x6000
	s_addc_u32 s1, s1, 0
	global_load_dword v221, v13, s[0:1]
	s_add_u32 s0, s0, 0x6000
	s_addc_u32 s1, s1, 0
	global_load_dword v222, v13, s[0:1]
	s_add_u32 s0, s0, 0x6000
	s_addc_u32 s1, s1, 0
	global_load_dword v223, v13, s[0:1]
	s_add_u32 s0, s0, 0x6000
	s_addc_u32 s1, s1, 0
	global_load_dword v224, v13, s[0:1]
	s_add_u32 s0, s0, 0x6000
	s_addc_u32 s1, s1, 0
	global_load_dword v225, v13, s[0:1]
	s_add_u32 s0, s0, 0x6000
	s_addc_u32 s1, s1, 0
	global_load_dword v226, v13, s[0:1]
	s_add_u32 s0, s0, 0x6000
	s_addc_u32 s1, s1, 0
	global_load_dword v227, v13, s[0:1]
	s_add_u32 s0, s0, 0x6000
	s_addc_u32 s1, s1, 0
	global_load_dword v228, v13, s[0:1]
	s_add_u32 s0, s0, 0x6000
	s_addc_u32 s1, s1, 0
	global_load_dword v229, v13, s[0:1]
	s_add_u32 s0, s0, 0x6000
	s_addc_u32 s1, s1, 0
	global_load_dword v230, v13, s[0:1]
	s_add_u32 s0, s0, 0x6000
	s_addc_u32 s1, s1, 0
	global_load_dword v231, v13, s[0:1]
	s_add_u32 s0, s0, 0x6000
	s_addc_u32 s1, s1, 0
	global_load_dword v232, v13, s[0:1]
	s_add_u32 s0, s0, 0x6000
	s_addc_u32 s1, s1, 0
	global_load_dword v233, v13, s[0:1]
	s_add_u32 s0, s0, 0x6000
	s_addc_u32 s1, s1, 0
	global_load_dword v234, v13, s[0:1]
	s_add_u32 s0, s0, 0x6000
	s_addc_u32 s1, s1, 0
	global_load_dword v235, v13, s[0:1]
	s_add_u32 s0, s0, 0x6000
	s_addc_u32 s1, s1, 0
	global_load_dword v236, v13, s[0:1]
	s_add_u32 s0, s0, 0x6000
	s_addc_u32 s1, s1, 0
	global_load_dword v237, v13, s[0:1]
	s_add_u32 s0, s0, 0x6000
	s_addc_u32 s1, s1, 0
	global_load_dword v238, v13, s[0:1]
	s_add_u32 s0, s0, 0x6000
	s_addc_u32 s1, s1, 0
	global_load_dword v239, v13, s[0:1]
	s_add_u32 s0, s0, 0x6000
	s_addc_u32 s1, s1, 0
	global_load_dword v240, v13, s[0:1]
	s_add_u32 s0, s0, 0x6000
	s_addc_u32 s1, s1, 0
	global_load_dword v241, v13, s[0:1]
	s_add_u32 s0, s0, 0x6000
	s_addc_u32 s1, s1, 0
	ds_read_b64 v[24:25], v14
	ds_read_b64 v[26:27], v14 offset:4096
	ds_read_b64 v[28:29], v14 offset:8192
	ds_read_b64 v[30:31], v14 offset:12288
	ds_read_b64 v[32:33], v14 offset:16384
	ds_read_b64 v[34:35], v14 offset:20480
	ds_read_b64 v[36:37], v14 offset:24576
	ds_read_b64 v[38:39], v14 offset:28672
	ds_read_b64 v[40:41], v14 offset:32768
	s_waitcnt lgkmcnt(0)
	ds_read_b64 v[42:43], v14 offset:8
	ds_read_b64 v[44:45], v14 offset:4104
	ds_read_b64 v[46:47], v14 offset:8200
	ds_read_b64 v[48:49], v14 offset:12296
	ds_read_b64 v[50:51], v14 offset:16392
	ds_read_b64 v[52:53], v14 offset:20488
	ds_read_b64 v[54:55], v14 offset:24584
	ds_read_b64 v[60:61], v14 offset:28680
	ds_read_b64 v[62:63], v14 offset:32776
	s_waitcnt vmcnt(44)
	v_fmac_f32_e32 v2, v24, v194
	v_fmac_f32_e32 v3, v26, v194
	v_fmac_f32_e32 v4, v28, v194
	v_fmac_f32_e32 v5, v30, v194
	v_fmac_f32_e32 v6, v32, v194
	v_fmac_f32_e32 v7, v34, v194
	v_fmac_f32_e32 v9, v36, v194
	v_fmac_f32_e32 v10, v38, v194
	v_fmac_f32_e32 v11, v40, v194
	v_fmac_f32_e32 v2, v25, v195
	v_fmac_f32_e32 v3, v27, v195
	v_fmac_f32_e32 v4, v29, v195
	v_fmac_f32_e32 v5, v31, v195
	v_fmac_f32_e32 v6, v33, v195
	v_fmac_f32_e32 v7, v35, v195
	v_fmac_f32_e32 v9, v37, v195
	v_fmac_f32_e32 v10, v39, v195
	v_fmac_f32_e32 v11, v41, v195
	s_waitcnt lgkmcnt(0)
	ds_read_b64 v[24:25], v14 offset:16
	ds_read_b64 v[26:27], v14 offset:4112
	ds_read_b64 v[28:29], v14 offset:8208
	ds_read_b64 v[30:31], v14 offset:12304
	ds_read_b64 v[32:33], v14 offset:16400
	ds_read_b64 v[34:35], v14 offset:20496
	ds_read_b64 v[36:37], v14 offset:24592
	ds_read_b64 v[38:39], v14 offset:28688
	ds_read_b64 v[40:41], v14 offset:32784
	v_fmac_f32_e32 v2, v42, v196
	v_fmac_f32_e32 v3, v44, v196
	v_fmac_f32_e32 v4, v46, v196
	v_fmac_f32_e32 v5, v48, v196
	v_fmac_f32_e32 v6, v50, v196
	v_fmac_f32_e32 v7, v52, v196
	v_fmac_f32_e32 v9, v54, v196
	v_fmac_f32_e32 v10, v60, v196
	v_fmac_f32_e32 v11, v62, v196
	v_fmac_f32_e32 v2, v43, v197
	v_fmac_f32_e32 v3, v45, v197
	v_fmac_f32_e32 v4, v47, v197
	v_fmac_f32_e32 v5, v49, v197
	v_fmac_f32_e32 v6, v51, v197
	v_fmac_f32_e32 v7, v53, v197
	v_fmac_f32_e32 v9, v55, v197
	v_fmac_f32_e32 v10, v61, v197
	v_fmac_f32_e32 v11, v63, v197
	global_load_dword v194, v13, s[0:1]
	s_add_u32 s0, s0, 0x6000
	s_addc_u32 s1, s1, 0
	global_load_dword v195, v13, s[0:1]
	s_add_u32 s0, s0, 0x6000
	s_addc_u32 s1, s1, 0
	global_load_dword v196, v13, s[0:1]
	s_add_u32 s0, s0, 0x6000
	s_addc_u32 s1, s1, 0
	global_load_dword v197, v13, s[0:1]
	s_add_u32 s0, s0, 0x6000
	s_addc_u32 s1, s1, 0
	s_waitcnt lgkmcnt(0)
	ds_read_b64 v[42:43], v14 offset:24
	ds_read_b64 v[44:45], v14 offset:4120
	ds_read_b64 v[46:47], v14 offset:8216
	ds_read_b64 v[48:49], v14 offset:12312
	ds_read_b64 v[50:51], v14 offset:16408
	ds_read_b64 v[52:53], v14 offset:20504
	ds_read_b64 v[54:55], v14 offset:24600
	ds_read_b64 v[60:61], v14 offset:28696
	ds_read_b64 v[62:63], v14 offset:32792
	s_waitcnt vmcnt(44)
	v_fmac_f32_e32 v2, v24, v198
	v_fmac_f32_e32 v3, v26, v198
	v_fmac_f32_e32 v4, v28, v198
	v_fmac_f32_e32 v5, v30, v198
	v_fmac_f32_e32 v6, v32, v198
	v_fmac_f32_e32 v7, v34, v198
	v_fmac_f32_e32 v9, v36, v198
	v_fmac_f32_e32 v10, v38, v198
	v_fmac_f32_e32 v11, v40, v198
	v_fmac_f32_e32 v2, v25, v199
	v_fmac_f32_e32 v3, v27, v199
	v_fmac_f32_e32 v4, v29, v199
	v_fmac_f32_e32 v5, v31, v199
	v_fmac_f32_e32 v6, v33, v199
	v_fmac_f32_e32 v7, v35, v199
	v_fmac_f32_e32 v9, v37, v199
	v_fmac_f32_e32 v10, v39, v199
	v_fmac_f32_e32 v11, v41, v199
	s_waitcnt lgkmcnt(0)
	ds_read_b64 v[24:25], v14 offset:32
	ds_read_b64 v[26:27], v14 offset:4128
	ds_read_b64 v[28:29], v14 offset:8224
	ds_read_b64 v[30:31], v14 offset:12320
	ds_read_b64 v[32:33], v14 offset:16416
	ds_read_b64 v[34:35], v14 offset:20512
	ds_read_b64 v[36:37], v14 offset:24608
	ds_read_b64 v[38:39], v14 offset:28704
	ds_read_b64 v[40:41], v14 offset:32800
	v_fmac_f32_e32 v2, v42, v200
	v_fmac_f32_e32 v3, v44, v200
	v_fmac_f32_e32 v4, v46, v200
	v_fmac_f32_e32 v5, v48, v200
	v_fmac_f32_e32 v6, v50, v200
	v_fmac_f32_e32 v7, v52, v200
	v_fmac_f32_e32 v9, v54, v200
	v_fmac_f32_e32 v10, v60, v200
	v_fmac_f32_e32 v11, v62, v200
	v_fmac_f32_e32 v2, v43, v201
	v_fmac_f32_e32 v3, v45, v201
	v_fmac_f32_e32 v4, v47, v201
	v_fmac_f32_e32 v5, v49, v201
	v_fmac_f32_e32 v6, v51, v201
	v_fmac_f32_e32 v7, v53, v201
	v_fmac_f32_e32 v9, v55, v201
	v_fmac_f32_e32 v10, v61, v201
	v_fmac_f32_e32 v11, v63, v201
	global_load_dword v198, v13, s[0:1]
	s_add_u32 s0, s0, 0x6000
	s_addc_u32 s1, s1, 0
	global_load_dword v199, v13, s[0:1]
	s_add_u32 s0, s0, 0x6000
	s_addc_u32 s1, s1, 0
	global_load_dword v200, v13, s[0:1]
	s_add_u32 s0, s0, 0x6000
	s_addc_u32 s1, s1, 0
	global_load_dword v201, v13, s[0:1]
	s_add_u32 s0, s0, 0x6000
	s_addc_u32 s1, s1, 0
	s_waitcnt lgkmcnt(0)
	ds_read_b64 v[42:43], v14 offset:40
	ds_read_b64 v[44:45], v14 offset:4136
	ds_read_b64 v[46:47], v14 offset:8232
	ds_read_b64 v[48:49], v14 offset:12328
	ds_read_b64 v[50:51], v14 offset:16424
	ds_read_b64 v[52:53], v14 offset:20520
	ds_read_b64 v[54:55], v14 offset:24616
	ds_read_b64 v[60:61], v14 offset:28712
	ds_read_b64 v[62:63], v14 offset:32808
	s_waitcnt vmcnt(44)
	v_fmac_f32_e32 v2, v24, v202
	v_fmac_f32_e32 v3, v26, v202
	v_fmac_f32_e32 v4, v28, v202
	v_fmac_f32_e32 v5, v30, v202
	v_fmac_f32_e32 v6, v32, v202
	v_fmac_f32_e32 v7, v34, v202
	v_fmac_f32_e32 v9, v36, v202
	v_fmac_f32_e32 v10, v38, v202
	v_fmac_f32_e32 v11, v40, v202
	v_fmac_f32_e32 v2, v25, v203
	v_fmac_f32_e32 v3, v27, v203
	v_fmac_f32_e32 v4, v29, v203
	v_fmac_f32_e32 v5, v31, v203
	v_fmac_f32_e32 v6, v33, v203
	v_fmac_f32_e32 v7, v35, v203
	v_fmac_f32_e32 v9, v37, v203
	v_fmac_f32_e32 v10, v39, v203
	v_fmac_f32_e32 v11, v41, v203
	s_waitcnt lgkmcnt(0)
	ds_read_b64 v[24:25], v14 offset:48
	ds_read_b64 v[26:27], v14 offset:4144
	ds_read_b64 v[28:29], v14 offset:8240
	ds_read_b64 v[30:31], v14 offset:12336
	ds_read_b64 v[32:33], v14 offset:16432
	ds_read_b64 v[34:35], v14 offset:20528
	ds_read_b64 v[36:37], v14 offset:24624
	ds_read_b64 v[38:39], v14 offset:28720
	ds_read_b64 v[40:41], v14 offset:32816
	v_fmac_f32_e32 v2, v42, v204
	v_fmac_f32_e32 v3, v44, v204
	v_fmac_f32_e32 v4, v46, v204
	v_fmac_f32_e32 v5, v48, v204
	v_fmac_f32_e32 v6, v50, v204
	v_fmac_f32_e32 v7, v52, v204
	v_fmac_f32_e32 v9, v54, v204
	v_fmac_f32_e32 v10, v60, v204
	v_fmac_f32_e32 v11, v62, v204
	v_fmac_f32_e32 v2, v43, v205
	v_fmac_f32_e32 v3, v45, v205
	v_fmac_f32_e32 v4, v47, v205
	v_fmac_f32_e32 v5, v49, v205
	v_fmac_f32_e32 v6, v51, v205
	v_fmac_f32_e32 v7, v53, v205
	v_fmac_f32_e32 v9, v55, v205
	v_fmac_f32_e32 v10, v61, v205
	v_fmac_f32_e32 v11, v63, v205
	global_load_dword v202, v13, s[0:1]
	s_add_u32 s0, s0, 0x6000
	s_addc_u32 s1, s1, 0
	global_load_dword v203, v13, s[0:1]
	s_add_u32 s0, s0, 0x6000
	s_addc_u32 s1, s1, 0
	global_load_dword v204, v13, s[0:1]
	s_add_u32 s0, s0, 0x6000
	s_addc_u32 s1, s1, 0
	global_load_dword v205, v13, s[0:1]
	s_add_u32 s0, s0, 0x6000
	s_addc_u32 s1, s1, 0
	s_waitcnt lgkmcnt(0)
	ds_read_b64 v[42:43], v14 offset:56
	ds_read_b64 v[44:45], v14 offset:4152
	ds_read_b64 v[46:47], v14 offset:8248
	ds_read_b64 v[48:49], v14 offset:12344
	ds_read_b64 v[50:51], v14 offset:16440
	ds_read_b64 v[52:53], v14 offset:20536
	ds_read_b64 v[54:55], v14 offset:24632
	ds_read_b64 v[60:61], v14 offset:28728
	ds_read_b64 v[62:63], v14 offset:32824
	s_waitcnt vmcnt(44)
	v_fmac_f32_e32 v2, v24, v206
	v_fmac_f32_e32 v3, v26, v206
	v_fmac_f32_e32 v4, v28, v206
	v_fmac_f32_e32 v5, v30, v206
	v_fmac_f32_e32 v6, v32, v206
	v_fmac_f32_e32 v7, v34, v206
	v_fmac_f32_e32 v9, v36, v206
	v_fmac_f32_e32 v10, v38, v206
	v_fmac_f32_e32 v11, v40, v206
	v_fmac_f32_e32 v2, v25, v207
	v_fmac_f32_e32 v3, v27, v207
	v_fmac_f32_e32 v4, v29, v207
	v_fmac_f32_e32 v5, v31, v207
	v_fmac_f32_e32 v6, v33, v207
	v_fmac_f32_e32 v7, v35, v207
	v_fmac_f32_e32 v9, v37, v207
	v_fmac_f32_e32 v10, v39, v207
	v_fmac_f32_e32 v11, v41, v207
	s_waitcnt lgkmcnt(0)
	ds_read_b64 v[24:25], v14 offset:64
	ds_read_b64 v[26:27], v14 offset:4160
	ds_read_b64 v[28:29], v14 offset:8256
	ds_read_b64 v[30:31], v14 offset:12352
	ds_read_b64 v[32:33], v14 offset:16448
	ds_read_b64 v[34:35], v14 offset:20544
	ds_read_b64 v[36:37], v14 offset:24640
	ds_read_b64 v[38:39], v14 offset:28736
	ds_read_b64 v[40:41], v14 offset:32832
	v_fmac_f32_e32 v2, v42, v208
	v_fmac_f32_e32 v3, v44, v208
	v_fmac_f32_e32 v4, v46, v208
	v_fmac_f32_e32 v5, v48, v208
	v_fmac_f32_e32 v6, v50, v208
	v_fmac_f32_e32 v7, v52, v208
	v_fmac_f32_e32 v9, v54, v208
	v_fmac_f32_e32 v10, v60, v208
	v_fmac_f32_e32 v11, v62, v208
	v_fmac_f32_e32 v2, v43, v209
	v_fmac_f32_e32 v3, v45, v209
	v_fmac_f32_e32 v4, v47, v209
	v_fmac_f32_e32 v5, v49, v209
	v_fmac_f32_e32 v6, v51, v209
	v_fmac_f32_e32 v7, v53, v209
	v_fmac_f32_e32 v9, v55, v209
	v_fmac_f32_e32 v10, v61, v209
	v_fmac_f32_e32 v11, v63, v209
	global_load_dword v206, v13, s[0:1]
	s_add_u32 s0, s0, 0x6000
	s_addc_u32 s1, s1, 0
	global_load_dword v207, v13, s[0:1]
	s_add_u32 s0, s0, 0x6000
	s_addc_u32 s1, s1, 0
	global_load_dword v208, v13, s[0:1]
	s_add_u32 s0, s0, 0x6000
	s_addc_u32 s1, s1, 0
	global_load_dword v209, v13, s[0:1]
	s_add_u32 s0, s0, 0x6000
	s_addc_u32 s1, s1, 0
	s_waitcnt lgkmcnt(0)
	ds_read_b64 v[42:43], v14 offset:72
	ds_read_b64 v[44:45], v14 offset:4168
	ds_read_b64 v[46:47], v14 offset:8264
	ds_read_b64 v[48:49], v14 offset:12360
	ds_read_b64 v[50:51], v14 offset:16456
	ds_read_b64 v[52:53], v14 offset:20552
	ds_read_b64 v[54:55], v14 offset:24648
	ds_read_b64 v[60:61], v14 offset:28744
	ds_read_b64 v[62:63], v14 offset:32840
	s_waitcnt vmcnt(44)
	v_fmac_f32_e32 v2, v24, v210
	v_fmac_f32_e32 v3, v26, v210
	v_fmac_f32_e32 v4, v28, v210
	v_fmac_f32_e32 v5, v30, v210
	v_fmac_f32_e32 v6, v32, v210
	v_fmac_f32_e32 v7, v34, v210
	v_fmac_f32_e32 v9, v36, v210
	v_fmac_f32_e32 v10, v38, v210
	v_fmac_f32_e32 v11, v40, v210
	v_fmac_f32_e32 v2, v25, v211
	v_fmac_f32_e32 v3, v27, v211
	v_fmac_f32_e32 v4, v29, v211
	v_fmac_f32_e32 v5, v31, v211
	v_fmac_f32_e32 v6, v33, v211
	v_fmac_f32_e32 v7, v35, v211
	v_fmac_f32_e32 v9, v37, v211
	v_fmac_f32_e32 v10, v39, v211
	v_fmac_f32_e32 v11, v41, v211
	s_waitcnt lgkmcnt(0)
	ds_read_b64 v[24:25], v14 offset:80
	ds_read_b64 v[26:27], v14 offset:4176
	ds_read_b64 v[28:29], v14 offset:8272
	ds_read_b64 v[30:31], v14 offset:12368
	ds_read_b64 v[32:33], v14 offset:16464
	ds_read_b64 v[34:35], v14 offset:20560
	ds_read_b64 v[36:37], v14 offset:24656
	ds_read_b64 v[38:39], v14 offset:28752
	ds_read_b64 v[40:41], v14 offset:32848
	v_fmac_f32_e32 v2, v42, v212
	v_fmac_f32_e32 v3, v44, v212
	v_fmac_f32_e32 v4, v46, v212
	v_fmac_f32_e32 v5, v48, v212
	v_fmac_f32_e32 v6, v50, v212
	v_fmac_f32_e32 v7, v52, v212
	v_fmac_f32_e32 v9, v54, v212
	v_fmac_f32_e32 v10, v60, v212
	v_fmac_f32_e32 v11, v62, v212
	v_fmac_f32_e32 v2, v43, v213
	v_fmac_f32_e32 v3, v45, v213
	v_fmac_f32_e32 v4, v47, v213
	v_fmac_f32_e32 v5, v49, v213
	v_fmac_f32_e32 v6, v51, v213
	v_fmac_f32_e32 v7, v53, v213
	v_fmac_f32_e32 v9, v55, v213
	v_fmac_f32_e32 v10, v61, v213
	v_fmac_f32_e32 v11, v63, v213
	global_load_dword v210, v13, s[0:1]
	s_add_u32 s0, s0, 0x6000
	s_addc_u32 s1, s1, 0
	global_load_dword v211, v13, s[0:1]
	s_add_u32 s0, s0, 0x6000
	s_addc_u32 s1, s1, 0
	global_load_dword v212, v13, s[0:1]
	s_add_u32 s0, s0, 0x6000
	s_addc_u32 s1, s1, 0
	global_load_dword v213, v13, s[0:1]
	s_add_u32 s0, s0, 0x6000
	s_addc_u32 s1, s1, 0
	s_waitcnt lgkmcnt(0)
	ds_read_b64 v[42:43], v14 offset:88
	ds_read_b64 v[44:45], v14 offset:4184
	ds_read_b64 v[46:47], v14 offset:8280
	ds_read_b64 v[48:49], v14 offset:12376
	ds_read_b64 v[50:51], v14 offset:16472
	ds_read_b64 v[52:53], v14 offset:20568
	ds_read_b64 v[54:55], v14 offset:24664
	ds_read_b64 v[60:61], v14 offset:28760
	ds_read_b64 v[62:63], v14 offset:32856
	s_waitcnt vmcnt(44)
	v_fmac_f32_e32 v2, v24, v214
	v_fmac_f32_e32 v3, v26, v214
	v_fmac_f32_e32 v4, v28, v214
	v_fmac_f32_e32 v5, v30, v214
	v_fmac_f32_e32 v6, v32, v214
	v_fmac_f32_e32 v7, v34, v214
	v_fmac_f32_e32 v9, v36, v214
	v_fmac_f32_e32 v10, v38, v214
	v_fmac_f32_e32 v11, v40, v214
	v_fmac_f32_e32 v2, v25, v215
	v_fmac_f32_e32 v3, v27, v215
	v_fmac_f32_e32 v4, v29, v215
	v_fmac_f32_e32 v5, v31, v215
	v_fmac_f32_e32 v6, v33, v215
	v_fmac_f32_e32 v7, v35, v215
	v_fmac_f32_e32 v9, v37, v215
	v_fmac_f32_e32 v10, v39, v215
	v_fmac_f32_e32 v11, v41, v215
	s_waitcnt lgkmcnt(0)
	ds_read_b64 v[24:25], v14 offset:96
	ds_read_b64 v[26:27], v14 offset:4192
	ds_read_b64 v[28:29], v14 offset:8288
	ds_read_b64 v[30:31], v14 offset:12384
	ds_read_b64 v[32:33], v14 offset:16480
	ds_read_b64 v[34:35], v14 offset:20576
	ds_read_b64 v[36:37], v14 offset:24672
	ds_read_b64 v[38:39], v14 offset:28768
	ds_read_b64 v[40:41], v14 offset:32864
	v_fmac_f32_e32 v2, v42, v216
	v_fmac_f32_e32 v3, v44, v216
	v_fmac_f32_e32 v4, v46, v216
	v_fmac_f32_e32 v5, v48, v216
	v_fmac_f32_e32 v6, v50, v216
	v_fmac_f32_e32 v7, v52, v216
	v_fmac_f32_e32 v9, v54, v216
	v_fmac_f32_e32 v10, v60, v216
	v_fmac_f32_e32 v11, v62, v216
	v_fmac_f32_e32 v2, v43, v217
	v_fmac_f32_e32 v3, v45, v217
	v_fmac_f32_e32 v4, v47, v217
	v_fmac_f32_e32 v5, v49, v217
	v_fmac_f32_e32 v6, v51, v217
	v_fmac_f32_e32 v7, v53, v217
	v_fmac_f32_e32 v9, v55, v217
	v_fmac_f32_e32 v10, v61, v217
	v_fmac_f32_e32 v11, v63, v217
	global_load_dword v214, v13, s[0:1]
	s_add_u32 s0, s0, 0x6000
	s_addc_u32 s1, s1, 0
	global_load_dword v215, v13, s[0:1]
	s_add_u32 s0, s0, 0x6000
	s_addc_u32 s1, s1, 0
	global_load_dword v216, v13, s[0:1]
	s_add_u32 s0, s0, 0x6000
	s_addc_u32 s1, s1, 0
	global_load_dword v217, v13, s[0:1]
	s_add_u32 s0, s0, 0x6000
	s_addc_u32 s1, s1, 0
	s_waitcnt lgkmcnt(0)
	ds_read_b64 v[42:43], v14 offset:104
	ds_read_b64 v[44:45], v14 offset:4200
	ds_read_b64 v[46:47], v14 offset:8296
	ds_read_b64 v[48:49], v14 offset:12392
	ds_read_b64 v[50:51], v14 offset:16488
	ds_read_b64 v[52:53], v14 offset:20584
	ds_read_b64 v[54:55], v14 offset:24680
	ds_read_b64 v[60:61], v14 offset:28776
	ds_read_b64 v[62:63], v14 offset:32872
	s_waitcnt vmcnt(44)
	v_fmac_f32_e32 v2, v24, v218
	v_fmac_f32_e32 v3, v26, v218
	v_fmac_f32_e32 v4, v28, v218
	v_fmac_f32_e32 v5, v30, v218
	v_fmac_f32_e32 v6, v32, v218
	v_fmac_f32_e32 v7, v34, v218
	v_fmac_f32_e32 v9, v36, v218
	v_fmac_f32_e32 v10, v38, v218
	v_fmac_f32_e32 v11, v40, v218
	v_fmac_f32_e32 v2, v25, v219
	v_fmac_f32_e32 v3, v27, v219
	v_fmac_f32_e32 v4, v29, v219
	v_fmac_f32_e32 v5, v31, v219
	v_fmac_f32_e32 v6, v33, v219
	v_fmac_f32_e32 v7, v35, v219
	v_fmac_f32_e32 v9, v37, v219
	v_fmac_f32_e32 v10, v39, v219
	v_fmac_f32_e32 v11, v41, v219
	s_waitcnt lgkmcnt(0)
	ds_read_b64 v[24:25], v14 offset:112
	ds_read_b64 v[26:27], v14 offset:4208
	ds_read_b64 v[28:29], v14 offset:8304
	ds_read_b64 v[30:31], v14 offset:12400
	ds_read_b64 v[32:33], v14 offset:16496
	ds_read_b64 v[34:35], v14 offset:20592
	ds_read_b64 v[36:37], v14 offset:24688
	ds_read_b64 v[38:39], v14 offset:28784
	ds_read_b64 v[40:41], v14 offset:32880
	v_fmac_f32_e32 v2, v42, v220
	v_fmac_f32_e32 v3, v44, v220
	v_fmac_f32_e32 v4, v46, v220
	v_fmac_f32_e32 v5, v48, v220
	v_fmac_f32_e32 v6, v50, v220
	v_fmac_f32_e32 v7, v52, v220
	v_fmac_f32_e32 v9, v54, v220
	v_fmac_f32_e32 v10, v60, v220
	v_fmac_f32_e32 v11, v62, v220
	v_fmac_f32_e32 v2, v43, v221
	v_fmac_f32_e32 v3, v45, v221
	v_fmac_f32_e32 v4, v47, v221
	v_fmac_f32_e32 v5, v49, v221
	v_fmac_f32_e32 v6, v51, v221
	v_fmac_f32_e32 v7, v53, v221
	v_fmac_f32_e32 v9, v55, v221
	v_fmac_f32_e32 v10, v61, v221
	v_fmac_f32_e32 v11, v63, v221
	global_load_dword v218, v13, s[0:1]
	s_add_u32 s0, s0, 0x6000
	s_addc_u32 s1, s1, 0
	global_load_dword v219, v13, s[0:1]
	s_add_u32 s0, s0, 0x6000
	s_addc_u32 s1, s1, 0
	global_load_dword v220, v13, s[0:1]
	s_add_u32 s0, s0, 0x6000
	s_addc_u32 s1, s1, 0
	global_load_dword v221, v13, s[0:1]
	s_add_u32 s0, s0, 0x6000
	s_addc_u32 s1, s1, 0
	s_waitcnt lgkmcnt(0)
	ds_read_b64 v[42:43], v14 offset:120
	ds_read_b64 v[44:45], v14 offset:4216
	ds_read_b64 v[46:47], v14 offset:8312
	ds_read_b64 v[48:49], v14 offset:12408
	ds_read_b64 v[50:51], v14 offset:16504
	ds_read_b64 v[52:53], v14 offset:20600
	ds_read_b64 v[54:55], v14 offset:24696
	ds_read_b64 v[60:61], v14 offset:28792
	ds_read_b64 v[62:63], v14 offset:32888
	s_waitcnt vmcnt(44)
	v_fmac_f32_e32 v2, v24, v222
	v_fmac_f32_e32 v3, v26, v222
	v_fmac_f32_e32 v4, v28, v222
	v_fmac_f32_e32 v5, v30, v222
	v_fmac_f32_e32 v6, v32, v222
	v_fmac_f32_e32 v7, v34, v222
	v_fmac_f32_e32 v9, v36, v222
	v_fmac_f32_e32 v10, v38, v222
	v_fmac_f32_e32 v11, v40, v222
	v_fmac_f32_e32 v2, v25, v223
	v_fmac_f32_e32 v3, v27, v223
	v_fmac_f32_e32 v4, v29, v223
	v_fmac_f32_e32 v5, v31, v223
	v_fmac_f32_e32 v6, v33, v223
	v_fmac_f32_e32 v7, v35, v223
	v_fmac_f32_e32 v9, v37, v223
	v_fmac_f32_e32 v10, v39, v223
	v_fmac_f32_e32 v11, v41, v223
	s_waitcnt lgkmcnt(0)
	ds_read_b64 v[24:25], v14 offset:128
	ds_read_b64 v[26:27], v14 offset:4224
	ds_read_b64 v[28:29], v14 offset:8320
	ds_read_b64 v[30:31], v14 offset:12416
	ds_read_b64 v[32:33], v14 offset:16512
	ds_read_b64 v[34:35], v14 offset:20608
	ds_read_b64 v[36:37], v14 offset:24704
	ds_read_b64 v[38:39], v14 offset:28800
	ds_read_b64 v[40:41], v14 offset:32896
	v_fmac_f32_e32 v2, v42, v224
	v_fmac_f32_e32 v3, v44, v224
	v_fmac_f32_e32 v4, v46, v224
	v_fmac_f32_e32 v5, v48, v224
	v_fmac_f32_e32 v6, v50, v224
	v_fmac_f32_e32 v7, v52, v224
	v_fmac_f32_e32 v9, v54, v224
	v_fmac_f32_e32 v10, v60, v224
	v_fmac_f32_e32 v11, v62, v224
	v_fmac_f32_e32 v2, v43, v225
	v_fmac_f32_e32 v3, v45, v225
	v_fmac_f32_e32 v4, v47, v225
	v_fmac_f32_e32 v5, v49, v225
	v_fmac_f32_e32 v6, v51, v225
	v_fmac_f32_e32 v7, v53, v225
	v_fmac_f32_e32 v9, v55, v225
	v_fmac_f32_e32 v10, v61, v225
	v_fmac_f32_e32 v11, v63, v225
	global_load_dword v222, v13, s[0:1]
	s_add_u32 s0, s0, 0x6000
	s_addc_u32 s1, s1, 0
	global_load_dword v223, v13, s[0:1]
	s_add_u32 s0, s0, 0x6000
	s_addc_u32 s1, s1, 0
	global_load_dword v224, v13, s[0:1]
	s_add_u32 s0, s0, 0x6000
	s_addc_u32 s1, s1, 0
	global_load_dword v225, v13, s[0:1]
	s_add_u32 s0, s0, 0x6000
	s_addc_u32 s1, s1, 0
	s_waitcnt lgkmcnt(0)
	ds_read_b64 v[42:43], v14 offset:136
	ds_read_b64 v[44:45], v14 offset:4232
	ds_read_b64 v[46:47], v14 offset:8328
	ds_read_b64 v[48:49], v14 offset:12424
	ds_read_b64 v[50:51], v14 offset:16520
	ds_read_b64 v[52:53], v14 offset:20616
	ds_read_b64 v[54:55], v14 offset:24712
	ds_read_b64 v[60:61], v14 offset:28808
	ds_read_b64 v[62:63], v14 offset:32904
	s_waitcnt vmcnt(44)
	v_fmac_f32_e32 v2, v24, v226
	v_fmac_f32_e32 v3, v26, v226
	v_fmac_f32_e32 v4, v28, v226
	v_fmac_f32_e32 v5, v30, v226
	v_fmac_f32_e32 v6, v32, v226
	v_fmac_f32_e32 v7, v34, v226
	v_fmac_f32_e32 v9, v36, v226
	v_fmac_f32_e32 v10, v38, v226
	v_fmac_f32_e32 v11, v40, v226
	v_fmac_f32_e32 v2, v25, v227
	v_fmac_f32_e32 v3, v27, v227
	v_fmac_f32_e32 v4, v29, v227
	v_fmac_f32_e32 v5, v31, v227
	v_fmac_f32_e32 v6, v33, v227
	v_fmac_f32_e32 v7, v35, v227
	v_fmac_f32_e32 v9, v37, v227
	v_fmac_f32_e32 v10, v39, v227
	v_fmac_f32_e32 v11, v41, v227
	s_waitcnt lgkmcnt(0)
	ds_read_b64 v[24:25], v14 offset:144
	ds_read_b64 v[26:27], v14 offset:4240
	ds_read_b64 v[28:29], v14 offset:8336
	ds_read_b64 v[30:31], v14 offset:12432
	ds_read_b64 v[32:33], v14 offset:16528
	ds_read_b64 v[34:35], v14 offset:20624
	ds_read_b64 v[36:37], v14 offset:24720
	ds_read_b64 v[38:39], v14 offset:28816
	ds_read_b64 v[40:41], v14 offset:32912
	v_fmac_f32_e32 v2, v42, v228
	v_fmac_f32_e32 v3, v44, v228
	v_fmac_f32_e32 v4, v46, v228
	v_fmac_f32_e32 v5, v48, v228
	v_fmac_f32_e32 v6, v50, v228
	v_fmac_f32_e32 v7, v52, v228
	v_fmac_f32_e32 v9, v54, v228
	v_fmac_f32_e32 v10, v60, v228
	v_fmac_f32_e32 v11, v62, v228
	v_fmac_f32_e32 v2, v43, v229
	v_fmac_f32_e32 v3, v45, v229
	v_fmac_f32_e32 v4, v47, v229
	v_fmac_f32_e32 v5, v49, v229
	v_fmac_f32_e32 v6, v51, v229
	v_fmac_f32_e32 v7, v53, v229
	v_fmac_f32_e32 v9, v55, v229
	v_fmac_f32_e32 v10, v61, v229
	v_fmac_f32_e32 v11, v63, v229
	global_load_dword v226, v13, s[0:1]
	s_add_u32 s0, s0, 0x6000
	s_addc_u32 s1, s1, 0
	global_load_dword v227, v13, s[0:1]
	s_add_u32 s0, s0, 0x6000
	s_addc_u32 s1, s1, 0
	global_load_dword v228, v13, s[0:1]
	s_add_u32 s0, s0, 0x6000
	s_addc_u32 s1, s1, 0
	global_load_dword v229, v13, s[0:1]
	s_add_u32 s0, s0, 0x6000
	s_addc_u32 s1, s1, 0
	s_waitcnt lgkmcnt(0)
	ds_read_b64 v[42:43], v14 offset:152
	ds_read_b64 v[44:45], v14 offset:4248
	ds_read_b64 v[46:47], v14 offset:8344
	ds_read_b64 v[48:49], v14 offset:12440
	ds_read_b64 v[50:51], v14 offset:16536
	ds_read_b64 v[52:53], v14 offset:20632
	ds_read_b64 v[54:55], v14 offset:24728
	ds_read_b64 v[60:61], v14 offset:28824
	ds_read_b64 v[62:63], v14 offset:32920
	s_waitcnt vmcnt(44)
	v_fmac_f32_e32 v2, v24, v230
	v_fmac_f32_e32 v3, v26, v230
	v_fmac_f32_e32 v4, v28, v230
	v_fmac_f32_e32 v5, v30, v230
	v_fmac_f32_e32 v6, v32, v230
	v_fmac_f32_e32 v7, v34, v230
	v_fmac_f32_e32 v9, v36, v230
	v_fmac_f32_e32 v10, v38, v230
	v_fmac_f32_e32 v11, v40, v230
	v_fmac_f32_e32 v2, v25, v231
	v_fmac_f32_e32 v3, v27, v231
	v_fmac_f32_e32 v4, v29, v231
	v_fmac_f32_e32 v5, v31, v231
	v_fmac_f32_e32 v6, v33, v231
	v_fmac_f32_e32 v7, v35, v231
	v_fmac_f32_e32 v9, v37, v231
	v_fmac_f32_e32 v10, v39, v231
	v_fmac_f32_e32 v11, v41, v231
	s_waitcnt lgkmcnt(0)
	ds_read_b64 v[24:25], v14 offset:160
	ds_read_b64 v[26:27], v14 offset:4256
	ds_read_b64 v[28:29], v14 offset:8352
	ds_read_b64 v[30:31], v14 offset:12448
	ds_read_b64 v[32:33], v14 offset:16544
	ds_read_b64 v[34:35], v14 offset:20640
	ds_read_b64 v[36:37], v14 offset:24736
	ds_read_b64 v[38:39], v14 offset:28832
	ds_read_b64 v[40:41], v14 offset:32928
	v_fmac_f32_e32 v2, v42, v232
	v_fmac_f32_e32 v3, v44, v232
	v_fmac_f32_e32 v4, v46, v232
	v_fmac_f32_e32 v5, v48, v232
	v_fmac_f32_e32 v6, v50, v232
	v_fmac_f32_e32 v7, v52, v232
	v_fmac_f32_e32 v9, v54, v232
	v_fmac_f32_e32 v10, v60, v232
	v_fmac_f32_e32 v11, v62, v232
	v_fmac_f32_e32 v2, v43, v233
	v_fmac_f32_e32 v3, v45, v233
	v_fmac_f32_e32 v4, v47, v233
	v_fmac_f32_e32 v5, v49, v233
	v_fmac_f32_e32 v6, v51, v233
	v_fmac_f32_e32 v7, v53, v233
	v_fmac_f32_e32 v9, v55, v233
	v_fmac_f32_e32 v10, v61, v233
	v_fmac_f32_e32 v11, v63, v233
	global_load_dword v230, v13, s[0:1]
	s_add_u32 s0, s0, 0x6000
	s_addc_u32 s1, s1, 0
	global_load_dword v231, v13, s[0:1]
	s_add_u32 s0, s0, 0x6000
	s_addc_u32 s1, s1, 0
	global_load_dword v232, v13, s[0:1]
	s_add_u32 s0, s0, 0x6000
	s_addc_u32 s1, s1, 0
	global_load_dword v233, v13, s[0:1]
	s_add_u32 s0, s0, 0x6000
	s_addc_u32 s1, s1, 0
	s_waitcnt lgkmcnt(0)
	ds_read_b64 v[42:43], v14 offset:168
	ds_read_b64 v[44:45], v14 offset:4264
	ds_read_b64 v[46:47], v14 offset:8360
	ds_read_b64 v[48:49], v14 offset:12456
	ds_read_b64 v[50:51], v14 offset:16552
	ds_read_b64 v[52:53], v14 offset:20648
	ds_read_b64 v[54:55], v14 offset:24744
	ds_read_b64 v[60:61], v14 offset:28840
	ds_read_b64 v[62:63], v14 offset:32936
	s_waitcnt vmcnt(44)
	v_fmac_f32_e32 v2, v24, v234
	v_fmac_f32_e32 v3, v26, v234
	v_fmac_f32_e32 v4, v28, v234
	v_fmac_f32_e32 v5, v30, v234
	v_fmac_f32_e32 v6, v32, v234
	v_fmac_f32_e32 v7, v34, v234
	v_fmac_f32_e32 v9, v36, v234
	v_fmac_f32_e32 v10, v38, v234
	v_fmac_f32_e32 v11, v40, v234
	v_fmac_f32_e32 v2, v25, v235
	v_fmac_f32_e32 v3, v27, v235
	v_fmac_f32_e32 v4, v29, v235
	v_fmac_f32_e32 v5, v31, v235
	v_fmac_f32_e32 v6, v33, v235
	v_fmac_f32_e32 v7, v35, v235
	v_fmac_f32_e32 v9, v37, v235
	v_fmac_f32_e32 v10, v39, v235
	v_fmac_f32_e32 v11, v41, v235
	s_waitcnt lgkmcnt(0)
	ds_read_b64 v[24:25], v14 offset:176
	ds_read_b64 v[26:27], v14 offset:4272
	ds_read_b64 v[28:29], v14 offset:8368
	ds_read_b64 v[30:31], v14 offset:12464
	ds_read_b64 v[32:33], v14 offset:16560
	ds_read_b64 v[34:35], v14 offset:20656
	ds_read_b64 v[36:37], v14 offset:24752
	ds_read_b64 v[38:39], v14 offset:28848
	ds_read_b64 v[40:41], v14 offset:32944
	v_fmac_f32_e32 v2, v42, v236
	v_fmac_f32_e32 v3, v44, v236
	v_fmac_f32_e32 v4, v46, v236
	v_fmac_f32_e32 v5, v48, v236
	v_fmac_f32_e32 v6, v50, v236
	v_fmac_f32_e32 v7, v52, v236
	v_fmac_f32_e32 v9, v54, v236
	v_fmac_f32_e32 v10, v60, v236
	v_fmac_f32_e32 v11, v62, v236
	v_fmac_f32_e32 v2, v43, v237
	v_fmac_f32_e32 v3, v45, v237
	v_fmac_f32_e32 v4, v47, v237
	v_fmac_f32_e32 v5, v49, v237
	v_fmac_f32_e32 v6, v51, v237
	v_fmac_f32_e32 v7, v53, v237
	v_fmac_f32_e32 v9, v55, v237
	v_fmac_f32_e32 v10, v61, v237
	v_fmac_f32_e32 v11, v63, v237
	global_load_dword v234, v13, s[0:1]
	s_add_u32 s0, s0, 0x6000
	s_addc_u32 s1, s1, 0
	global_load_dword v235, v13, s[0:1]
	s_add_u32 s0, s0, 0x6000
	s_addc_u32 s1, s1, 0
	global_load_dword v236, v13, s[0:1]
	s_add_u32 s0, s0, 0x6000
	s_addc_u32 s1, s1, 0
	global_load_dword v237, v13, s[0:1]
	s_add_u32 s0, s0, 0x6000
	s_addc_u32 s1, s1, 0
	s_waitcnt lgkmcnt(0)
	ds_read_b64 v[42:43], v14 offset:184
	ds_read_b64 v[44:45], v14 offset:4280
	ds_read_b64 v[46:47], v14 offset:8376
	ds_read_b64 v[48:49], v14 offset:12472
	ds_read_b64 v[50:51], v14 offset:16568
	ds_read_b64 v[52:53], v14 offset:20664
	ds_read_b64 v[54:55], v14 offset:24760
	ds_read_b64 v[60:61], v14 offset:28856
	ds_read_b64 v[62:63], v14 offset:32952
	s_waitcnt vmcnt(44)
	v_fmac_f32_e32 v2, v24, v238
	v_fmac_f32_e32 v3, v26, v238
	v_fmac_f32_e32 v4, v28, v238
	v_fmac_f32_e32 v5, v30, v238
	v_fmac_f32_e32 v6, v32, v238
	v_fmac_f32_e32 v7, v34, v238
	v_fmac_f32_e32 v9, v36, v238
	v_fmac_f32_e32 v10, v38, v238
	v_fmac_f32_e32 v11, v40, v238
	v_fmac_f32_e32 v2, v25, v239
	v_fmac_f32_e32 v3, v27, v239
	v_fmac_f32_e32 v4, v29, v239
	v_fmac_f32_e32 v5, v31, v239
	v_fmac_f32_e32 v6, v33, v239
	v_fmac_f32_e32 v7, v35, v239
	v_fmac_f32_e32 v9, v37, v239
	v_fmac_f32_e32 v10, v39, v239
	v_fmac_f32_e32 v11, v41, v239
	s_waitcnt lgkmcnt(0)
	ds_read_b64 v[24:25], v14 offset:192
	ds_read_b64 v[26:27], v14 offset:4288
	ds_read_b64 v[28:29], v14 offset:8384
	ds_read_b64 v[30:31], v14 offset:12480
	ds_read_b64 v[32:33], v14 offset:16576
	ds_read_b64 v[34:35], v14 offset:20672
	ds_read_b64 v[36:37], v14 offset:24768
	ds_read_b64 v[38:39], v14 offset:28864
	ds_read_b64 v[40:41], v14 offset:32960
	v_fmac_f32_e32 v2, v42, v240
	v_fmac_f32_e32 v3, v44, v240
	v_fmac_f32_e32 v4, v46, v240
	v_fmac_f32_e32 v5, v48, v240
	v_fmac_f32_e32 v6, v50, v240
	v_fmac_f32_e32 v7, v52, v240
	v_fmac_f32_e32 v9, v54, v240
	v_fmac_f32_e32 v10, v60, v240
	v_fmac_f32_e32 v11, v62, v240
	v_fmac_f32_e32 v2, v43, v241
	v_fmac_f32_e32 v3, v45, v241
	v_fmac_f32_e32 v4, v47, v241
	v_fmac_f32_e32 v5, v49, v241
	v_fmac_f32_e32 v6, v51, v241
	v_fmac_f32_e32 v7, v53, v241
	v_fmac_f32_e32 v9, v55, v241
	v_fmac_f32_e32 v10, v61, v241
	v_fmac_f32_e32 v11, v63, v241
	global_load_dword v238, v13, s[0:1]
	s_add_u32 s0, s0, 0x6000
	s_addc_u32 s1, s1, 0
	global_load_dword v239, v13, s[0:1]
	s_add_u32 s0, s0, 0x6000
	s_addc_u32 s1, s1, 0
	global_load_dword v240, v13, s[0:1]
	s_add_u32 s0, s0, 0x6000
	s_addc_u32 s1, s1, 0
	global_load_dword v241, v13, s[0:1]
	s_add_u32 s0, s0, 0x6000
	s_addc_u32 s1, s1, 0
	s_waitcnt lgkmcnt(0)
	ds_read_b64 v[42:43], v14 offset:200
	ds_read_b64 v[44:45], v14 offset:4296
	ds_read_b64 v[46:47], v14 offset:8392
	ds_read_b64 v[48:49], v14 offset:12488
	ds_read_b64 v[50:51], v14 offset:16584
	ds_read_b64 v[52:53], v14 offset:20680
	ds_read_b64 v[54:55], v14 offset:24776
	ds_read_b64 v[60:61], v14 offset:28872
	ds_read_b64 v[62:63], v14 offset:32968
	s_waitcnt vmcnt(44)
	v_fmac_f32_e32 v2, v24, v194
	v_fmac_f32_e32 v3, v26, v194
	v_fmac_f32_e32 v4, v28, v194
	v_fmac_f32_e32 v5, v30, v194
	v_fmac_f32_e32 v6, v32, v194
	v_fmac_f32_e32 v7, v34, v194
	v_fmac_f32_e32 v9, v36, v194
	v_fmac_f32_e32 v10, v38, v194
	v_fmac_f32_e32 v11, v40, v194
	v_fmac_f32_e32 v2, v25, v195
	v_fmac_f32_e32 v3, v27, v195
	v_fmac_f32_e32 v4, v29, v195
	v_fmac_f32_e32 v5, v31, v195
	v_fmac_f32_e32 v6, v33, v195
	v_fmac_f32_e32 v7, v35, v195
	v_fmac_f32_e32 v9, v37, v195
	v_fmac_f32_e32 v10, v39, v195
	v_fmac_f32_e32 v11, v41, v195
	s_waitcnt lgkmcnt(0)
	ds_read_b64 v[24:25], v14 offset:208
	ds_read_b64 v[26:27], v14 offset:4304
	ds_read_b64 v[28:29], v14 offset:8400
	ds_read_b64 v[30:31], v14 offset:12496
	ds_read_b64 v[32:33], v14 offset:16592
	ds_read_b64 v[34:35], v14 offset:20688
	ds_read_b64 v[36:37], v14 offset:24784
	ds_read_b64 v[38:39], v14 offset:28880
	ds_read_b64 v[40:41], v14 offset:32976
	v_fmac_f32_e32 v2, v42, v196
	v_fmac_f32_e32 v3, v44, v196
	v_fmac_f32_e32 v4, v46, v196
	v_fmac_f32_e32 v5, v48, v196
	v_fmac_f32_e32 v6, v50, v196
	v_fmac_f32_e32 v7, v52, v196
	v_fmac_f32_e32 v9, v54, v196
	v_fmac_f32_e32 v10, v60, v196
	v_fmac_f32_e32 v11, v62, v196
	v_fmac_f32_e32 v2, v43, v197
	v_fmac_f32_e32 v3, v45, v197
	v_fmac_f32_e32 v4, v47, v197
	v_fmac_f32_e32 v5, v49, v197
	v_fmac_f32_e32 v6, v51, v197
	v_fmac_f32_e32 v7, v53, v197
	v_fmac_f32_e32 v9, v55, v197
	v_fmac_f32_e32 v10, v61, v197
	v_fmac_f32_e32 v11, v63, v197
	global_load_dword v194, v13, s[0:1]
	s_add_u32 s0, s0, 0x6000
	s_addc_u32 s1, s1, 0
	global_load_dword v195, v13, s[0:1]
	s_add_u32 s0, s0, 0x6000
	s_addc_u32 s1, s1, 0
	global_load_dword v196, v13, s[0:1]
	s_add_u32 s0, s0, 0x6000
	s_addc_u32 s1, s1, 0
	global_load_dword v197, v13, s[0:1]
	s_add_u32 s0, s0, 0x6000
	s_addc_u32 s1, s1, 0
	s_waitcnt lgkmcnt(0)
	ds_read_b64 v[42:43], v14 offset:216
	ds_read_b64 v[44:45], v14 offset:4312
	ds_read_b64 v[46:47], v14 offset:8408
	ds_read_b64 v[48:49], v14 offset:12504
	ds_read_b64 v[50:51], v14 offset:16600
	ds_read_b64 v[52:53], v14 offset:20696
	ds_read_b64 v[54:55], v14 offset:24792
	ds_read_b64 v[60:61], v14 offset:28888
	ds_read_b64 v[62:63], v14 offset:32984
	s_waitcnt vmcnt(44)
	v_fmac_f32_e32 v2, v24, v198
	v_fmac_f32_e32 v3, v26, v198
	v_fmac_f32_e32 v4, v28, v198
	v_fmac_f32_e32 v5, v30, v198
	v_fmac_f32_e32 v6, v32, v198
	v_fmac_f32_e32 v7, v34, v198
	v_fmac_f32_e32 v9, v36, v198
	v_fmac_f32_e32 v10, v38, v198
	v_fmac_f32_e32 v11, v40, v198
	v_fmac_f32_e32 v2, v25, v199
	v_fmac_f32_e32 v3, v27, v199
	v_fmac_f32_e32 v4, v29, v199
	v_fmac_f32_e32 v5, v31, v199
	v_fmac_f32_e32 v6, v33, v199
	v_fmac_f32_e32 v7, v35, v199
	v_fmac_f32_e32 v9, v37, v199
	v_fmac_f32_e32 v10, v39, v199
	v_fmac_f32_e32 v11, v41, v199
	s_waitcnt lgkmcnt(0)
	ds_read_b64 v[24:25], v14 offset:224
	ds_read_b64 v[26:27], v14 offset:4320
	ds_read_b64 v[28:29], v14 offset:8416
	ds_read_b64 v[30:31], v14 offset:12512
	ds_read_b64 v[32:33], v14 offset:16608
	ds_read_b64 v[34:35], v14 offset:20704
	ds_read_b64 v[36:37], v14 offset:24800
	ds_read_b64 v[38:39], v14 offset:28896
	ds_read_b64 v[40:41], v14 offset:32992
	v_fmac_f32_e32 v2, v42, v200
	v_fmac_f32_e32 v3, v44, v200
	v_fmac_f32_e32 v4, v46, v200
	v_fmac_f32_e32 v5, v48, v200
	v_fmac_f32_e32 v6, v50, v200
	v_fmac_f32_e32 v7, v52, v200
	v_fmac_f32_e32 v9, v54, v200
	v_fmac_f32_e32 v10, v60, v200
	v_fmac_f32_e32 v11, v62, v200
	v_fmac_f32_e32 v2, v43, v201
	v_fmac_f32_e32 v3, v45, v201
	v_fmac_f32_e32 v4, v47, v201
	v_fmac_f32_e32 v5, v49, v201
	v_fmac_f32_e32 v6, v51, v201
	v_fmac_f32_e32 v7, v53, v201
	v_fmac_f32_e32 v9, v55, v201
	v_fmac_f32_e32 v10, v61, v201
	v_fmac_f32_e32 v11, v63, v201
	global_load_dword v198, v13, s[0:1]
	s_add_u32 s0, s0, 0x6000
	s_addc_u32 s1, s1, 0
	global_load_dword v199, v13, s[0:1]
	s_add_u32 s0, s0, 0x6000
	s_addc_u32 s1, s1, 0
	global_load_dword v200, v13, s[0:1]
	s_add_u32 s0, s0, 0x6000
	s_addc_u32 s1, s1, 0
	global_load_dword v201, v13, s[0:1]
	s_add_u32 s0, s0, 0x6000
	s_addc_u32 s1, s1, 0
	s_waitcnt lgkmcnt(0)
	ds_read_b64 v[42:43], v14 offset:232
	ds_read_b64 v[44:45], v14 offset:4328
	ds_read_b64 v[46:47], v14 offset:8424
	ds_read_b64 v[48:49], v14 offset:12520
	ds_read_b64 v[50:51], v14 offset:16616
	ds_read_b64 v[52:53], v14 offset:20712
	ds_read_b64 v[54:55], v14 offset:24808
	ds_read_b64 v[60:61], v14 offset:28904
	ds_read_b64 v[62:63], v14 offset:33000
	s_waitcnt vmcnt(44)
	v_fmac_f32_e32 v2, v24, v202
	v_fmac_f32_e32 v3, v26, v202
	v_fmac_f32_e32 v4, v28, v202
	v_fmac_f32_e32 v5, v30, v202
	v_fmac_f32_e32 v6, v32, v202
	v_fmac_f32_e32 v7, v34, v202
	v_fmac_f32_e32 v9, v36, v202
	v_fmac_f32_e32 v10, v38, v202
	v_fmac_f32_e32 v11, v40, v202
	v_fmac_f32_e32 v2, v25, v203
	v_fmac_f32_e32 v3, v27, v203
	v_fmac_f32_e32 v4, v29, v203
	v_fmac_f32_e32 v5, v31, v203
	v_fmac_f32_e32 v6, v33, v203
	v_fmac_f32_e32 v7, v35, v203
	v_fmac_f32_e32 v9, v37, v203
	v_fmac_f32_e32 v10, v39, v203
	v_fmac_f32_e32 v11, v41, v203
	s_waitcnt lgkmcnt(0)
	ds_read_b64 v[24:25], v14 offset:240
	ds_read_b64 v[26:27], v14 offset:4336
	ds_read_b64 v[28:29], v14 offset:8432
	ds_read_b64 v[30:31], v14 offset:12528
	ds_read_b64 v[32:33], v14 offset:16624
	ds_read_b64 v[34:35], v14 offset:20720
	ds_read_b64 v[36:37], v14 offset:24816
	ds_read_b64 v[38:39], v14 offset:28912
	ds_read_b64 v[40:41], v14 offset:33008
	v_fmac_f32_e32 v2, v42, v204
	v_fmac_f32_e32 v3, v44, v204
	v_fmac_f32_e32 v4, v46, v204
	v_fmac_f32_e32 v5, v48, v204
	v_fmac_f32_e32 v6, v50, v204
	v_fmac_f32_e32 v7, v52, v204
	v_fmac_f32_e32 v9, v54, v204
	v_fmac_f32_e32 v10, v60, v204
	v_fmac_f32_e32 v11, v62, v204
	v_fmac_f32_e32 v2, v43, v205
	v_fmac_f32_e32 v3, v45, v205
	v_fmac_f32_e32 v4, v47, v205
	v_fmac_f32_e32 v5, v49, v205
	v_fmac_f32_e32 v6, v51, v205
	v_fmac_f32_e32 v7, v53, v205
	v_fmac_f32_e32 v9, v55, v205
	v_fmac_f32_e32 v10, v61, v205
	v_fmac_f32_e32 v11, v63, v205
	global_load_dword v202, v13, s[0:1]
	s_add_u32 s0, s0, 0x6000
	s_addc_u32 s1, s1, 0
	global_load_dword v203, v13, s[0:1]
	s_add_u32 s0, s0, 0x6000
	s_addc_u32 s1, s1, 0
	global_load_dword v204, v13, s[0:1]
	s_add_u32 s0, s0, 0x6000
	s_addc_u32 s1, s1, 0
	global_load_dword v205, v13, s[0:1]
	s_add_u32 s0, s0, 0x6000
	s_addc_u32 s1, s1, 0
	s_waitcnt lgkmcnt(0)
	ds_read_b64 v[42:43], v14 offset:248
	ds_read_b64 v[44:45], v14 offset:4344
	ds_read_b64 v[46:47], v14 offset:8440
	ds_read_b64 v[48:49], v14 offset:12536
	ds_read_b64 v[50:51], v14 offset:16632
	ds_read_b64 v[52:53], v14 offset:20728
	ds_read_b64 v[54:55], v14 offset:24824
	ds_read_b64 v[60:61], v14 offset:28920
	ds_read_b64 v[62:63], v14 offset:33016
	s_waitcnt vmcnt(44)
	v_fmac_f32_e32 v2, v24, v206
	v_fmac_f32_e32 v3, v26, v206
	v_fmac_f32_e32 v4, v28, v206
	v_fmac_f32_e32 v5, v30, v206
	v_fmac_f32_e32 v6, v32, v206
	v_fmac_f32_e32 v7, v34, v206
	v_fmac_f32_e32 v9, v36, v206
	v_fmac_f32_e32 v10, v38, v206
	v_fmac_f32_e32 v11, v40, v206
	v_fmac_f32_e32 v2, v25, v207
	v_fmac_f32_e32 v3, v27, v207
	v_fmac_f32_e32 v4, v29, v207
	v_fmac_f32_e32 v5, v31, v207
	v_fmac_f32_e32 v6, v33, v207
	v_fmac_f32_e32 v7, v35, v207
	v_fmac_f32_e32 v9, v37, v207
	v_fmac_f32_e32 v10, v39, v207
	v_fmac_f32_e32 v11, v41, v207
	s_waitcnt lgkmcnt(0)
	ds_read_b64 v[24:25], v14 offset:256
	ds_read_b64 v[26:27], v14 offset:4352
	ds_read_b64 v[28:29], v14 offset:8448
	ds_read_b64 v[30:31], v14 offset:12544
	ds_read_b64 v[32:33], v14 offset:16640
	ds_read_b64 v[34:35], v14 offset:20736
	ds_read_b64 v[36:37], v14 offset:24832
	ds_read_b64 v[38:39], v14 offset:28928
	ds_read_b64 v[40:41], v14 offset:33024
	v_fmac_f32_e32 v2, v42, v208
	v_fmac_f32_e32 v3, v44, v208
	v_fmac_f32_e32 v4, v46, v208
	v_fmac_f32_e32 v5, v48, v208
	v_fmac_f32_e32 v6, v50, v208
	v_fmac_f32_e32 v7, v52, v208
	v_fmac_f32_e32 v9, v54, v208
	v_fmac_f32_e32 v10, v60, v208
	v_fmac_f32_e32 v11, v62, v208
	v_fmac_f32_e32 v2, v43, v209
	v_fmac_f32_e32 v3, v45, v209
	v_fmac_f32_e32 v4, v47, v209
	v_fmac_f32_e32 v5, v49, v209
	v_fmac_f32_e32 v6, v51, v209
	v_fmac_f32_e32 v7, v53, v209
	v_fmac_f32_e32 v9, v55, v209
	v_fmac_f32_e32 v10, v61, v209
	v_fmac_f32_e32 v11, v63, v209
	global_load_dword v206, v13, s[0:1]
	s_add_u32 s0, s0, 0x6000
	s_addc_u32 s1, s1, 0
	global_load_dword v207, v13, s[0:1]
	s_add_u32 s0, s0, 0x6000
	s_addc_u32 s1, s1, 0
	global_load_dword v208, v13, s[0:1]
	s_add_u32 s0, s0, 0x6000
	s_addc_u32 s1, s1, 0
	global_load_dword v209, v13, s[0:1]
	s_add_u32 s0, s0, 0x6000
	s_addc_u32 s1, s1, 0
	s_waitcnt lgkmcnt(0)
	ds_read_b64 v[42:43], v14 offset:264
	ds_read_b64 v[44:45], v14 offset:4360
	ds_read_b64 v[46:47], v14 offset:8456
	ds_read_b64 v[48:49], v14 offset:12552
	ds_read_b64 v[50:51], v14 offset:16648
	ds_read_b64 v[52:53], v14 offset:20744
	ds_read_b64 v[54:55], v14 offset:24840
	ds_read_b64 v[60:61], v14 offset:28936
	ds_read_b64 v[62:63], v14 offset:33032
	s_waitcnt vmcnt(44)
	v_fmac_f32_e32 v2, v24, v210
	v_fmac_f32_e32 v3, v26, v210
	v_fmac_f32_e32 v4, v28, v210
	v_fmac_f32_e32 v5, v30, v210
	v_fmac_f32_e32 v6, v32, v210
	v_fmac_f32_e32 v7, v34, v210
	v_fmac_f32_e32 v9, v36, v210
	v_fmac_f32_e32 v10, v38, v210
	v_fmac_f32_e32 v11, v40, v210
	v_fmac_f32_e32 v2, v25, v211
	v_fmac_f32_e32 v3, v27, v211
	v_fmac_f32_e32 v4, v29, v211
	v_fmac_f32_e32 v5, v31, v211
	v_fmac_f32_e32 v6, v33, v211
	v_fmac_f32_e32 v7, v35, v211
	v_fmac_f32_e32 v9, v37, v211
	v_fmac_f32_e32 v10, v39, v211
	v_fmac_f32_e32 v11, v41, v211
	s_waitcnt lgkmcnt(0)
	ds_read_b64 v[24:25], v14 offset:272
	ds_read_b64 v[26:27], v14 offset:4368
	ds_read_b64 v[28:29], v14 offset:8464
	ds_read_b64 v[30:31], v14 offset:12560
	ds_read_b64 v[32:33], v14 offset:16656
	ds_read_b64 v[34:35], v14 offset:20752
	ds_read_b64 v[36:37], v14 offset:24848
	ds_read_b64 v[38:39], v14 offset:28944
	ds_read_b64 v[40:41], v14 offset:33040
	v_fmac_f32_e32 v2, v42, v212
	v_fmac_f32_e32 v3, v44, v212
	v_fmac_f32_e32 v4, v46, v212
	v_fmac_f32_e32 v5, v48, v212
	v_fmac_f32_e32 v6, v50, v212
	v_fmac_f32_e32 v7, v52, v212
	v_fmac_f32_e32 v9, v54, v212
	v_fmac_f32_e32 v10, v60, v212
	v_fmac_f32_e32 v11, v62, v212
	v_fmac_f32_e32 v2, v43, v213
	v_fmac_f32_e32 v3, v45, v213
	v_fmac_f32_e32 v4, v47, v213
	v_fmac_f32_e32 v5, v49, v213
	v_fmac_f32_e32 v6, v51, v213
	v_fmac_f32_e32 v7, v53, v213
	v_fmac_f32_e32 v9, v55, v213
	v_fmac_f32_e32 v10, v61, v213
	v_fmac_f32_e32 v11, v63, v213
	global_load_dword v210, v13, s[0:1]
	s_add_u32 s0, s0, 0x6000
	s_addc_u32 s1, s1, 0
	global_load_dword v211, v13, s[0:1]
	s_add_u32 s0, s0, 0x6000
	s_addc_u32 s1, s1, 0
	global_load_dword v212, v13, s[0:1]
	s_add_u32 s0, s0, 0x6000
	s_addc_u32 s1, s1, 0
	global_load_dword v213, v13, s[0:1]
	s_add_u32 s0, s0, 0x6000
	s_addc_u32 s1, s1, 0
	s_waitcnt lgkmcnt(0)
	ds_read_b64 v[42:43], v14 offset:280
	ds_read_b64 v[44:45], v14 offset:4376
	ds_read_b64 v[46:47], v14 offset:8472
	ds_read_b64 v[48:49], v14 offset:12568
	ds_read_b64 v[50:51], v14 offset:16664
	ds_read_b64 v[52:53], v14 offset:20760
	ds_read_b64 v[54:55], v14 offset:24856
	ds_read_b64 v[60:61], v14 offset:28952
	ds_read_b64 v[62:63], v14 offset:33048
	s_waitcnt vmcnt(44)
	v_fmac_f32_e32 v2, v24, v214
	v_fmac_f32_e32 v3, v26, v214
	v_fmac_f32_e32 v4, v28, v214
	v_fmac_f32_e32 v5, v30, v214
	v_fmac_f32_e32 v6, v32, v214
	v_fmac_f32_e32 v7, v34, v214
	v_fmac_f32_e32 v9, v36, v214
	v_fmac_f32_e32 v10, v38, v214
	v_fmac_f32_e32 v11, v40, v214
	v_fmac_f32_e32 v2, v25, v215
	v_fmac_f32_e32 v3, v27, v215
	v_fmac_f32_e32 v4, v29, v215
	v_fmac_f32_e32 v5, v31, v215
	v_fmac_f32_e32 v6, v33, v215
	v_fmac_f32_e32 v7, v35, v215
	v_fmac_f32_e32 v9, v37, v215
	v_fmac_f32_e32 v10, v39, v215
	v_fmac_f32_e32 v11, v41, v215
	s_waitcnt lgkmcnt(0)
	ds_read_b64 v[24:25], v14 offset:288
	ds_read_b64 v[26:27], v14 offset:4384
	ds_read_b64 v[28:29], v14 offset:8480
	ds_read_b64 v[30:31], v14 offset:12576
	ds_read_b64 v[32:33], v14 offset:16672
	ds_read_b64 v[34:35], v14 offset:20768
	ds_read_b64 v[36:37], v14 offset:24864
	ds_read_b64 v[38:39], v14 offset:28960
	ds_read_b64 v[40:41], v14 offset:33056
	v_fmac_f32_e32 v2, v42, v216
	v_fmac_f32_e32 v3, v44, v216
	v_fmac_f32_e32 v4, v46, v216
	v_fmac_f32_e32 v5, v48, v216
	v_fmac_f32_e32 v6, v50, v216
	v_fmac_f32_e32 v7, v52, v216
	v_fmac_f32_e32 v9, v54, v216
	v_fmac_f32_e32 v10, v60, v216
	v_fmac_f32_e32 v11, v62, v216
	v_fmac_f32_e32 v2, v43, v217
	v_fmac_f32_e32 v3, v45, v217
	v_fmac_f32_e32 v4, v47, v217
	v_fmac_f32_e32 v5, v49, v217
	v_fmac_f32_e32 v6, v51, v217
	v_fmac_f32_e32 v7, v53, v217
	v_fmac_f32_e32 v9, v55, v217
	v_fmac_f32_e32 v10, v61, v217
	v_fmac_f32_e32 v11, v63, v217
	global_load_dword v214, v13, s[0:1]
	s_add_u32 s0, s0, 0x6000
	s_addc_u32 s1, s1, 0
	global_load_dword v215, v13, s[0:1]
	s_add_u32 s0, s0, 0x6000
	s_addc_u32 s1, s1, 0
	global_load_dword v216, v13, s[0:1]
	s_add_u32 s0, s0, 0x6000
	s_addc_u32 s1, s1, 0
	global_load_dword v217, v13, s[0:1]
	s_add_u32 s0, s0, 0x6000
	s_addc_u32 s1, s1, 0
	s_waitcnt lgkmcnt(0)
	ds_read_b64 v[42:43], v14 offset:296
	ds_read_b64 v[44:45], v14 offset:4392
	ds_read_b64 v[46:47], v14 offset:8488
	ds_read_b64 v[48:49], v14 offset:12584
	ds_read_b64 v[50:51], v14 offset:16680
	ds_read_b64 v[52:53], v14 offset:20776
	ds_read_b64 v[54:55], v14 offset:24872
	ds_read_b64 v[60:61], v14 offset:28968
	ds_read_b64 v[62:63], v14 offset:33064
	s_waitcnt vmcnt(44)
	v_fmac_f32_e32 v2, v24, v218
	v_fmac_f32_e32 v3, v26, v218
	v_fmac_f32_e32 v4, v28, v218
	v_fmac_f32_e32 v5, v30, v218
	v_fmac_f32_e32 v6, v32, v218
	v_fmac_f32_e32 v7, v34, v218
	v_fmac_f32_e32 v9, v36, v218
	v_fmac_f32_e32 v10, v38, v218
	v_fmac_f32_e32 v11, v40, v218
	v_fmac_f32_e32 v2, v25, v219
	v_fmac_f32_e32 v3, v27, v219
	v_fmac_f32_e32 v4, v29, v219
	v_fmac_f32_e32 v5, v31, v219
	v_fmac_f32_e32 v6, v33, v219
	v_fmac_f32_e32 v7, v35, v219
	v_fmac_f32_e32 v9, v37, v219
	v_fmac_f32_e32 v10, v39, v219
	v_fmac_f32_e32 v11, v41, v219
	s_waitcnt lgkmcnt(0)
	ds_read_b64 v[24:25], v14 offset:304
	ds_read_b64 v[26:27], v14 offset:4400
	ds_read_b64 v[28:29], v14 offset:8496
	ds_read_b64 v[30:31], v14 offset:12592
	ds_read_b64 v[32:33], v14 offset:16688
	ds_read_b64 v[34:35], v14 offset:20784
	ds_read_b64 v[36:37], v14 offset:24880
	ds_read_b64 v[38:39], v14 offset:28976
	ds_read_b64 v[40:41], v14 offset:33072
	v_fmac_f32_e32 v2, v42, v220
	v_fmac_f32_e32 v3, v44, v220
	v_fmac_f32_e32 v4, v46, v220
	v_fmac_f32_e32 v5, v48, v220
	v_fmac_f32_e32 v6, v50, v220
	v_fmac_f32_e32 v7, v52, v220
	v_fmac_f32_e32 v9, v54, v220
	v_fmac_f32_e32 v10, v60, v220
	v_fmac_f32_e32 v11, v62, v220
	v_fmac_f32_e32 v2, v43, v221
	v_fmac_f32_e32 v3, v45, v221
	v_fmac_f32_e32 v4, v47, v221
	v_fmac_f32_e32 v5, v49, v221
	v_fmac_f32_e32 v6, v51, v221
	v_fmac_f32_e32 v7, v53, v221
	v_fmac_f32_e32 v9, v55, v221
	v_fmac_f32_e32 v10, v61, v221
	v_fmac_f32_e32 v11, v63, v221
	global_load_dword v218, v13, s[0:1]
	s_add_u32 s0, s0, 0x6000
	s_addc_u32 s1, s1, 0
	global_load_dword v219, v13, s[0:1]
	s_add_u32 s0, s0, 0x6000
	s_addc_u32 s1, s1, 0
	global_load_dword v220, v13, s[0:1]
	s_add_u32 s0, s0, 0x6000
	s_addc_u32 s1, s1, 0
	global_load_dword v221, v13, s[0:1]
	s_add_u32 s0, s0, 0x6000
	s_addc_u32 s1, s1, 0
	s_waitcnt lgkmcnt(0)
	ds_read_b64 v[42:43], v14 offset:312
	ds_read_b64 v[44:45], v14 offset:4408
	ds_read_b64 v[46:47], v14 offset:8504
	ds_read_b64 v[48:49], v14 offset:12600
	ds_read_b64 v[50:51], v14 offset:16696
	ds_read_b64 v[52:53], v14 offset:20792
	ds_read_b64 v[54:55], v14 offset:24888
	ds_read_b64 v[60:61], v14 offset:28984
	ds_read_b64 v[62:63], v14 offset:33080
	s_waitcnt vmcnt(44)
	v_fmac_f32_e32 v2, v24, v222
	v_fmac_f32_e32 v3, v26, v222
	v_fmac_f32_e32 v4, v28, v222
	v_fmac_f32_e32 v5, v30, v222
	v_fmac_f32_e32 v6, v32, v222
	v_fmac_f32_e32 v7, v34, v222
	v_fmac_f32_e32 v9, v36, v222
	v_fmac_f32_e32 v10, v38, v222
	v_fmac_f32_e32 v11, v40, v222
	v_fmac_f32_e32 v2, v25, v223
	v_fmac_f32_e32 v3, v27, v223
	v_fmac_f32_e32 v4, v29, v223
	v_fmac_f32_e32 v5, v31, v223
	v_fmac_f32_e32 v6, v33, v223
	v_fmac_f32_e32 v7, v35, v223
	v_fmac_f32_e32 v9, v37, v223
	v_fmac_f32_e32 v10, v39, v223
	v_fmac_f32_e32 v11, v41, v223
	s_waitcnt lgkmcnt(0)
	ds_read_b64 v[24:25], v14 offset:320
	ds_read_b64 v[26:27], v14 offset:4416
	ds_read_b64 v[28:29], v14 offset:8512
	ds_read_b64 v[30:31], v14 offset:12608
	ds_read_b64 v[32:33], v14 offset:16704
	ds_read_b64 v[34:35], v14 offset:20800
	ds_read_b64 v[36:37], v14 offset:24896
	ds_read_b64 v[38:39], v14 offset:28992
	ds_read_b64 v[40:41], v14 offset:33088
	v_fmac_f32_e32 v2, v42, v224
	v_fmac_f32_e32 v3, v44, v224
	v_fmac_f32_e32 v4, v46, v224
	v_fmac_f32_e32 v5, v48, v224
	v_fmac_f32_e32 v6, v50, v224
	v_fmac_f32_e32 v7, v52, v224
	v_fmac_f32_e32 v9, v54, v224
	v_fmac_f32_e32 v10, v60, v224
	v_fmac_f32_e32 v11, v62, v224
	v_fmac_f32_e32 v2, v43, v225
	v_fmac_f32_e32 v3, v45, v225
	v_fmac_f32_e32 v4, v47, v225
	v_fmac_f32_e32 v5, v49, v225
	v_fmac_f32_e32 v6, v51, v225
	v_fmac_f32_e32 v7, v53, v225
	v_fmac_f32_e32 v9, v55, v225
	v_fmac_f32_e32 v10, v61, v225
	v_fmac_f32_e32 v11, v63, v225
	global_load_dword v222, v13, s[0:1]
	s_add_u32 s0, s0, 0x6000
	s_addc_u32 s1, s1, 0
	global_load_dword v223, v13, s[0:1]
	s_add_u32 s0, s0, 0x6000
	s_addc_u32 s1, s1, 0
	global_load_dword v224, v13, s[0:1]
	s_add_u32 s0, s0, 0x6000
	s_addc_u32 s1, s1, 0
	global_load_dword v225, v13, s[0:1]
	s_waitcnt lgkmcnt(0)
	ds_read_b64 v[42:43], v14 offset:328
	ds_read_b64 v[44:45], v14 offset:4424
	ds_read_b64 v[46:47], v14 offset:8520
	ds_read_b64 v[48:49], v14 offset:12616
	ds_read_b64 v[50:51], v14 offset:16712
	ds_read_b64 v[52:53], v14 offset:20808
	ds_read_b64 v[54:55], v14 offset:24904
	ds_read_b64 v[60:61], v14 offset:29000
	ds_read_b64 v[62:63], v14 offset:33096
	s_waitcnt vmcnt(44)
	v_fmac_f32_e32 v2, v24, v226
	v_fmac_f32_e32 v3, v26, v226
	v_fmac_f32_e32 v4, v28, v226
	v_fmac_f32_e32 v5, v30, v226
	v_fmac_f32_e32 v6, v32, v226
	v_fmac_f32_e32 v7, v34, v226
	v_fmac_f32_e32 v9, v36, v226
	v_fmac_f32_e32 v10, v38, v226
	v_fmac_f32_e32 v11, v40, v226
	v_fmac_f32_e32 v2, v25, v227
	v_fmac_f32_e32 v3, v27, v227
	v_fmac_f32_e32 v4, v29, v227
	v_fmac_f32_e32 v5, v31, v227
	v_fmac_f32_e32 v6, v33, v227
	v_fmac_f32_e32 v7, v35, v227
	v_fmac_f32_e32 v9, v37, v227
	v_fmac_f32_e32 v10, v39, v227
	v_fmac_f32_e32 v11, v41, v227
	s_waitcnt lgkmcnt(0)
	ds_read_b64 v[24:25], v14 offset:336
	ds_read_b64 v[26:27], v14 offset:4432
	ds_read_b64 v[28:29], v14 offset:8528
	ds_read_b64 v[30:31], v14 offset:12624
	ds_read_b64 v[32:33], v14 offset:16720
	ds_read_b64 v[34:35], v14 offset:20816
	ds_read_b64 v[36:37], v14 offset:24912
	ds_read_b64 v[38:39], v14 offset:29008
	ds_read_b64 v[40:41], v14 offset:33104
	v_fmac_f32_e32 v2, v42, v228
	v_fmac_f32_e32 v3, v44, v228
	v_fmac_f32_e32 v4, v46, v228
	v_fmac_f32_e32 v5, v48, v228
	v_fmac_f32_e32 v6, v50, v228
	v_fmac_f32_e32 v7, v52, v228
	v_fmac_f32_e32 v9, v54, v228
	v_fmac_f32_e32 v10, v60, v228
	v_fmac_f32_e32 v11, v62, v228
	v_fmac_f32_e32 v2, v43, v229
	v_fmac_f32_e32 v3, v45, v229
	v_fmac_f32_e32 v4, v47, v229
	v_fmac_f32_e32 v5, v49, v229
	v_fmac_f32_e32 v6, v51, v229
	v_fmac_f32_e32 v7, v53, v229
	v_fmac_f32_e32 v9, v55, v229
	v_fmac_f32_e32 v10, v61, v229
	v_fmac_f32_e32 v11, v63, v229
	s_waitcnt lgkmcnt(0)
	ds_read_b64 v[42:43], v14 offset:344
	ds_read_b64 v[44:45], v14 offset:4440
	ds_read_b64 v[46:47], v14 offset:8536
	ds_read_b64 v[48:49], v14 offset:12632
	ds_read_b64 v[50:51], v14 offset:16728
	ds_read_b64 v[52:53], v14 offset:20824
	ds_read_b64 v[54:55], v14 offset:24920
	ds_read_b64 v[60:61], v14 offset:29016
	ds_read_b64 v[62:63], v14 offset:33112
	s_waitcnt vmcnt(40)
	v_fmac_f32_e32 v2, v24, v230
	v_fmac_f32_e32 v3, v26, v230
	v_fmac_f32_e32 v4, v28, v230
	v_fmac_f32_e32 v5, v30, v230
	v_fmac_f32_e32 v6, v32, v230
	v_fmac_f32_e32 v7, v34, v230
	v_fmac_f32_e32 v9, v36, v230
	v_fmac_f32_e32 v10, v38, v230
	v_fmac_f32_e32 v11, v40, v230
	v_fmac_f32_e32 v2, v25, v231
	v_fmac_f32_e32 v3, v27, v231
	v_fmac_f32_e32 v4, v29, v231
	v_fmac_f32_e32 v5, v31, v231
	v_fmac_f32_e32 v6, v33, v231
	v_fmac_f32_e32 v7, v35, v231
	v_fmac_f32_e32 v9, v37, v231
	v_fmac_f32_e32 v10, v39, v231
	v_fmac_f32_e32 v11, v41, v231
	s_waitcnt lgkmcnt(0)
	ds_read_b64 v[24:25], v14 offset:352
	ds_read_b64 v[26:27], v14 offset:4448
	ds_read_b64 v[28:29], v14 offset:8544
	ds_read_b64 v[30:31], v14 offset:12640
	ds_read_b64 v[32:33], v14 offset:16736
	ds_read_b64 v[34:35], v14 offset:20832
	ds_read_b64 v[36:37], v14 offset:24928
	ds_read_b64 v[38:39], v14 offset:29024
	ds_read_b64 v[40:41], v14 offset:33120
	v_fmac_f32_e32 v2, v42, v232
	v_fmac_f32_e32 v3, v44, v232
	v_fmac_f32_e32 v4, v46, v232
	v_fmac_f32_e32 v5, v48, v232
	v_fmac_f32_e32 v6, v50, v232
	v_fmac_f32_e32 v7, v52, v232
	v_fmac_f32_e32 v9, v54, v232
	v_fmac_f32_e32 v10, v60, v232
	v_fmac_f32_e32 v11, v62, v232
	v_fmac_f32_e32 v2, v43, v233
	v_fmac_f32_e32 v3, v45, v233
	v_fmac_f32_e32 v4, v47, v233
	v_fmac_f32_e32 v5, v49, v233
	v_fmac_f32_e32 v6, v51, v233
	v_fmac_f32_e32 v7, v53, v233
	v_fmac_f32_e32 v9, v55, v233
	v_fmac_f32_e32 v10, v61, v233
	v_fmac_f32_e32 v11, v63, v233
	s_waitcnt lgkmcnt(0)
	ds_read_b64 v[42:43], v14 offset:360
	ds_read_b64 v[44:45], v14 offset:4456
	ds_read_b64 v[46:47], v14 offset:8552
	ds_read_b64 v[48:49], v14 offset:12648
	ds_read_b64 v[50:51], v14 offset:16744
	ds_read_b64 v[52:53], v14 offset:20840
	ds_read_b64 v[54:55], v14 offset:24936
	ds_read_b64 v[60:61], v14 offset:29032
	ds_read_b64 v[62:63], v14 offset:33128
	s_waitcnt vmcnt(36)
	v_fmac_f32_e32 v2, v24, v234
	v_fmac_f32_e32 v3, v26, v234
	v_fmac_f32_e32 v4, v28, v234
	v_fmac_f32_e32 v5, v30, v234
	v_fmac_f32_e32 v6, v32, v234
	v_fmac_f32_e32 v7, v34, v234
	v_fmac_f32_e32 v9, v36, v234
	v_fmac_f32_e32 v10, v38, v234
	v_fmac_f32_e32 v11, v40, v234
	v_fmac_f32_e32 v2, v25, v235
	v_fmac_f32_e32 v3, v27, v235
	v_fmac_f32_e32 v4, v29, v235
	v_fmac_f32_e32 v5, v31, v235
	v_fmac_f32_e32 v6, v33, v235
	v_fmac_f32_e32 v7, v35, v235
	v_fmac_f32_e32 v9, v37, v235
	v_fmac_f32_e32 v10, v39, v235
	v_fmac_f32_e32 v11, v41, v235
	s_waitcnt lgkmcnt(0)
	ds_read_b64 v[24:25], v14 offset:368
	ds_read_b64 v[26:27], v14 offset:4464
	ds_read_b64 v[28:29], v14 offset:8560
	ds_read_b64 v[30:31], v14 offset:12656
	ds_read_b64 v[32:33], v14 offset:16752
	ds_read_b64 v[34:35], v14 offset:20848
	ds_read_b64 v[36:37], v14 offset:24944
	ds_read_b64 v[38:39], v14 offset:29040
	ds_read_b64 v[40:41], v14 offset:33136
	v_fmac_f32_e32 v2, v42, v236
	v_fmac_f32_e32 v3, v44, v236
	v_fmac_f32_e32 v4, v46, v236
	v_fmac_f32_e32 v5, v48, v236
	v_fmac_f32_e32 v6, v50, v236
	v_fmac_f32_e32 v7, v52, v236
	v_fmac_f32_e32 v9, v54, v236
	v_fmac_f32_e32 v10, v60, v236
	v_fmac_f32_e32 v11, v62, v236
	v_fmac_f32_e32 v2, v43, v237
	v_fmac_f32_e32 v3, v45, v237
	v_fmac_f32_e32 v4, v47, v237
	v_fmac_f32_e32 v5, v49, v237
	v_fmac_f32_e32 v6, v51, v237
	v_fmac_f32_e32 v7, v53, v237
	v_fmac_f32_e32 v9, v55, v237
	v_fmac_f32_e32 v10, v61, v237
	v_fmac_f32_e32 v11, v63, v237
	s_waitcnt lgkmcnt(0)
	ds_read_b64 v[42:43], v14 offset:376
	ds_read_b64 v[44:45], v14 offset:4472
	ds_read_b64 v[46:47], v14 offset:8568
	ds_read_b64 v[48:49], v14 offset:12664
	ds_read_b64 v[50:51], v14 offset:16760
	ds_read_b64 v[52:53], v14 offset:20856
	ds_read_b64 v[54:55], v14 offset:24952
	ds_read_b64 v[60:61], v14 offset:29048
	ds_read_b64 v[62:63], v14 offset:33144
	s_waitcnt vmcnt(32)
	v_fmac_f32_e32 v2, v24, v238
	v_fmac_f32_e32 v3, v26, v238
	v_fmac_f32_e32 v4, v28, v238
	v_fmac_f32_e32 v5, v30, v238
	v_fmac_f32_e32 v6, v32, v238
	v_fmac_f32_e32 v7, v34, v238
	v_fmac_f32_e32 v9, v36, v238
	v_fmac_f32_e32 v10, v38, v238
	v_fmac_f32_e32 v11, v40, v238
	v_fmac_f32_e32 v2, v25, v239
	v_fmac_f32_e32 v3, v27, v239
	v_fmac_f32_e32 v4, v29, v239
	v_fmac_f32_e32 v5, v31, v239
	v_fmac_f32_e32 v6, v33, v239
	v_fmac_f32_e32 v7, v35, v239
	v_fmac_f32_e32 v9, v37, v239
	v_fmac_f32_e32 v10, v39, v239
	v_fmac_f32_e32 v11, v41, v239
	s_waitcnt lgkmcnt(0)
	ds_read_b64 v[24:25], v14 offset:384
	ds_read_b64 v[26:27], v14 offset:4480
	ds_read_b64 v[28:29], v14 offset:8576
	ds_read_b64 v[30:31], v14 offset:12672
	ds_read_b64 v[32:33], v14 offset:16768
	ds_read_b64 v[34:35], v14 offset:20864
	ds_read_b64 v[36:37], v14 offset:24960
	ds_read_b64 v[38:39], v14 offset:29056
	ds_read_b64 v[40:41], v14 offset:33152
	v_fmac_f32_e32 v2, v42, v240
	v_fmac_f32_e32 v3, v44, v240
	v_fmac_f32_e32 v4, v46, v240
	v_fmac_f32_e32 v5, v48, v240
	v_fmac_f32_e32 v6, v50, v240
	v_fmac_f32_e32 v7, v52, v240
	v_fmac_f32_e32 v9, v54, v240
	v_fmac_f32_e32 v10, v60, v240
	v_fmac_f32_e32 v11, v62, v240
	v_fmac_f32_e32 v2, v43, v241
	v_fmac_f32_e32 v3, v45, v241
	v_fmac_f32_e32 v4, v47, v241
	v_fmac_f32_e32 v5, v49, v241
	v_fmac_f32_e32 v6, v51, v241
	v_fmac_f32_e32 v7, v53, v241
	v_fmac_f32_e32 v9, v55, v241
	v_fmac_f32_e32 v10, v61, v241
	v_fmac_f32_e32 v11, v63, v241
	s_waitcnt lgkmcnt(0)
	ds_read_b64 v[42:43], v14 offset:392
	ds_read_b64 v[44:45], v14 offset:4488
	ds_read_b64 v[46:47], v14 offset:8584
	ds_read_b64 v[48:49], v14 offset:12680
	ds_read_b64 v[50:51], v14 offset:16776
	ds_read_b64 v[52:53], v14 offset:20872
	ds_read_b64 v[54:55], v14 offset:24968
	ds_read_b64 v[60:61], v14 offset:29064
	ds_read_b64 v[62:63], v14 offset:33160
	s_waitcnt vmcnt(28)
	v_fmac_f32_e32 v2, v24, v194
	v_fmac_f32_e32 v3, v26, v194
	v_fmac_f32_e32 v4, v28, v194
	v_fmac_f32_e32 v5, v30, v194
	v_fmac_f32_e32 v6, v32, v194
	v_fmac_f32_e32 v7, v34, v194
	v_fmac_f32_e32 v9, v36, v194
	v_fmac_f32_e32 v10, v38, v194
	v_fmac_f32_e32 v11, v40, v194
	v_fmac_f32_e32 v2, v25, v195
	v_fmac_f32_e32 v3, v27, v195
	v_fmac_f32_e32 v4, v29, v195
	v_fmac_f32_e32 v5, v31, v195
	v_fmac_f32_e32 v6, v33, v195
	v_fmac_f32_e32 v7, v35, v195
	v_fmac_f32_e32 v9, v37, v195
	v_fmac_f32_e32 v10, v39, v195
	v_fmac_f32_e32 v11, v41, v195
	s_waitcnt lgkmcnt(0)
	ds_read_b64 v[24:25], v14 offset:400
	ds_read_b64 v[26:27], v14 offset:4496
	ds_read_b64 v[28:29], v14 offset:8592
	ds_read_b64 v[30:31], v14 offset:12688
	ds_read_b64 v[32:33], v14 offset:16784
	ds_read_b64 v[34:35], v14 offset:20880
	ds_read_b64 v[36:37], v14 offset:24976
	ds_read_b64 v[38:39], v14 offset:29072
	ds_read_b64 v[40:41], v14 offset:33168
	v_fmac_f32_e32 v2, v42, v196
	v_fmac_f32_e32 v3, v44, v196
	v_fmac_f32_e32 v4, v46, v196
	v_fmac_f32_e32 v5, v48, v196
	v_fmac_f32_e32 v6, v50, v196
	v_fmac_f32_e32 v7, v52, v196
	v_fmac_f32_e32 v9, v54, v196
	v_fmac_f32_e32 v10, v60, v196
	v_fmac_f32_e32 v11, v62, v196
	v_fmac_f32_e32 v2, v43, v197
	v_fmac_f32_e32 v3, v45, v197
	v_fmac_f32_e32 v4, v47, v197
	v_fmac_f32_e32 v5, v49, v197
	v_fmac_f32_e32 v6, v51, v197
	v_fmac_f32_e32 v7, v53, v197
	v_fmac_f32_e32 v9, v55, v197
	v_fmac_f32_e32 v10, v61, v197
	v_fmac_f32_e32 v11, v63, v197
	s_waitcnt lgkmcnt(0)
	ds_read_b64 v[42:43], v14 offset:408
	ds_read_b64 v[44:45], v14 offset:4504
	ds_read_b64 v[46:47], v14 offset:8600
	ds_read_b64 v[48:49], v14 offset:12696
	ds_read_b64 v[50:51], v14 offset:16792
	ds_read_b64 v[52:53], v14 offset:20888
	ds_read_b64 v[54:55], v14 offset:24984
	ds_read_b64 v[60:61], v14 offset:29080
	ds_read_b64 v[62:63], v14 offset:33176
	s_waitcnt vmcnt(24)
	v_fmac_f32_e32 v2, v24, v198
	v_fmac_f32_e32 v3, v26, v198
	v_fmac_f32_e32 v4, v28, v198
	v_fmac_f32_e32 v5, v30, v198
	v_fmac_f32_e32 v6, v32, v198
	v_fmac_f32_e32 v7, v34, v198
	v_fmac_f32_e32 v9, v36, v198
	v_fmac_f32_e32 v10, v38, v198
	v_fmac_f32_e32 v11, v40, v198
	v_fmac_f32_e32 v2, v25, v199
	v_fmac_f32_e32 v3, v27, v199
	v_fmac_f32_e32 v4, v29, v199
	v_fmac_f32_e32 v5, v31, v199
	v_fmac_f32_e32 v6, v33, v199
	v_fmac_f32_e32 v7, v35, v199
	v_fmac_f32_e32 v9, v37, v199
	v_fmac_f32_e32 v10, v39, v199
	v_fmac_f32_e32 v11, v41, v199
	s_waitcnt lgkmcnt(0)
	ds_read_b64 v[24:25], v14 offset:416
	ds_read_b64 v[26:27], v14 offset:4512
	ds_read_b64 v[28:29], v14 offset:8608
	ds_read_b64 v[30:31], v14 offset:12704
	ds_read_b64 v[32:33], v14 offset:16800
	ds_read_b64 v[34:35], v14 offset:20896
	ds_read_b64 v[36:37], v14 offset:24992
	ds_read_b64 v[38:39], v14 offset:29088
	ds_read_b64 v[40:41], v14 offset:33184
	v_fmac_f32_e32 v2, v42, v200
	v_fmac_f32_e32 v3, v44, v200
	v_fmac_f32_e32 v4, v46, v200
	v_fmac_f32_e32 v5, v48, v200
	v_fmac_f32_e32 v6, v50, v200
	v_fmac_f32_e32 v7, v52, v200
	v_fmac_f32_e32 v9, v54, v200
	v_fmac_f32_e32 v10, v60, v200
	v_fmac_f32_e32 v11, v62, v200
	v_fmac_f32_e32 v2, v43, v201
	v_fmac_f32_e32 v3, v45, v201
	v_fmac_f32_e32 v4, v47, v201
	v_fmac_f32_e32 v5, v49, v201
	v_fmac_f32_e32 v6, v51, v201
	v_fmac_f32_e32 v7, v53, v201
	v_fmac_f32_e32 v9, v55, v201
	v_fmac_f32_e32 v10, v61, v201
	v_fmac_f32_e32 v11, v63, v201
	s_waitcnt lgkmcnt(0)
	ds_read_b64 v[42:43], v14 offset:424
	ds_read_b64 v[44:45], v14 offset:4520
	ds_read_b64 v[46:47], v14 offset:8616
	ds_read_b64 v[48:49], v14 offset:12712
	ds_read_b64 v[50:51], v14 offset:16808
	ds_read_b64 v[52:53], v14 offset:20904
	ds_read_b64 v[54:55], v14 offset:25000
	ds_read_b64 v[60:61], v14 offset:29096
	ds_read_b64 v[62:63], v14 offset:33192
	s_waitcnt vmcnt(20)
	v_fmac_f32_e32 v2, v24, v202
	v_fmac_f32_e32 v3, v26, v202
	v_fmac_f32_e32 v4, v28, v202
	v_fmac_f32_e32 v5, v30, v202
	v_fmac_f32_e32 v6, v32, v202
	v_fmac_f32_e32 v7, v34, v202
	v_fmac_f32_e32 v9, v36, v202
	v_fmac_f32_e32 v10, v38, v202
	v_fmac_f32_e32 v11, v40, v202
	v_fmac_f32_e32 v2, v25, v203
	v_fmac_f32_e32 v3, v27, v203
	v_fmac_f32_e32 v4, v29, v203
	v_fmac_f32_e32 v5, v31, v203
	v_fmac_f32_e32 v6, v33, v203
	v_fmac_f32_e32 v7, v35, v203
	v_fmac_f32_e32 v9, v37, v203
	v_fmac_f32_e32 v10, v39, v203
	v_fmac_f32_e32 v11, v41, v203
	s_waitcnt lgkmcnt(0)
	ds_read_b64 v[24:25], v14 offset:432
	ds_read_b64 v[26:27], v14 offset:4528
	ds_read_b64 v[28:29], v14 offset:8624
	ds_read_b64 v[30:31], v14 offset:12720
	ds_read_b64 v[32:33], v14 offset:16816
	ds_read_b64 v[34:35], v14 offset:20912
	ds_read_b64 v[36:37], v14 offset:25008
	ds_read_b64 v[38:39], v14 offset:29104
	ds_read_b64 v[40:41], v14 offset:33200
	v_fmac_f32_e32 v2, v42, v204
	v_fmac_f32_e32 v3, v44, v204
	v_fmac_f32_e32 v4, v46, v204
	v_fmac_f32_e32 v5, v48, v204
	v_fmac_f32_e32 v6, v50, v204
	v_fmac_f32_e32 v7, v52, v204
	v_fmac_f32_e32 v9, v54, v204
	v_fmac_f32_e32 v10, v60, v204
	v_fmac_f32_e32 v11, v62, v204
	v_fmac_f32_e32 v2, v43, v205
	v_fmac_f32_e32 v3, v45, v205
	v_fmac_f32_e32 v4, v47, v205
	v_fmac_f32_e32 v5, v49, v205
	v_fmac_f32_e32 v6, v51, v205
	v_fmac_f32_e32 v7, v53, v205
	v_fmac_f32_e32 v9, v55, v205
	v_fmac_f32_e32 v10, v61, v205
	v_fmac_f32_e32 v11, v63, v205
	s_waitcnt lgkmcnt(0)
	ds_read_b64 v[42:43], v14 offset:440
	ds_read_b64 v[44:45], v14 offset:4536
	ds_read_b64 v[46:47], v14 offset:8632
	ds_read_b64 v[48:49], v14 offset:12728
	ds_read_b64 v[50:51], v14 offset:16824
	ds_read_b64 v[52:53], v14 offset:20920
	ds_read_b64 v[54:55], v14 offset:25016
	ds_read_b64 v[60:61], v14 offset:29112
	ds_read_b64 v[62:63], v14 offset:33208
	s_waitcnt vmcnt(16)
	v_fmac_f32_e32 v2, v24, v206
	v_fmac_f32_e32 v3, v26, v206
	v_fmac_f32_e32 v4, v28, v206
	v_fmac_f32_e32 v5, v30, v206
	v_fmac_f32_e32 v6, v32, v206
	v_fmac_f32_e32 v7, v34, v206
	v_fmac_f32_e32 v9, v36, v206
	v_fmac_f32_e32 v10, v38, v206
	v_fmac_f32_e32 v11, v40, v206
	v_fmac_f32_e32 v2, v25, v207
	v_fmac_f32_e32 v3, v27, v207
	v_fmac_f32_e32 v4, v29, v207
	v_fmac_f32_e32 v5, v31, v207
	v_fmac_f32_e32 v6, v33, v207
	v_fmac_f32_e32 v7, v35, v207
	v_fmac_f32_e32 v9, v37, v207
	v_fmac_f32_e32 v10, v39, v207
	v_fmac_f32_e32 v11, v41, v207
	s_waitcnt lgkmcnt(0)
	ds_read_b64 v[24:25], v14 offset:448
	ds_read_b64 v[26:27], v14 offset:4544
	ds_read_b64 v[28:29], v14 offset:8640
	ds_read_b64 v[30:31], v14 offset:12736
	ds_read_b64 v[32:33], v14 offset:16832
	ds_read_b64 v[34:35], v14 offset:20928
	ds_read_b64 v[36:37], v14 offset:25024
	ds_read_b64 v[38:39], v14 offset:29120
	ds_read_b64 v[40:41], v14 offset:33216
	v_fmac_f32_e32 v2, v42, v208
	v_fmac_f32_e32 v3, v44, v208
	v_fmac_f32_e32 v4, v46, v208
	v_fmac_f32_e32 v5, v48, v208
	v_fmac_f32_e32 v6, v50, v208
	v_fmac_f32_e32 v7, v52, v208
	v_fmac_f32_e32 v9, v54, v208
	v_fmac_f32_e32 v10, v60, v208
	v_fmac_f32_e32 v11, v62, v208
	v_fmac_f32_e32 v2, v43, v209
	v_fmac_f32_e32 v3, v45, v209
	v_fmac_f32_e32 v4, v47, v209
	v_fmac_f32_e32 v5, v49, v209
	v_fmac_f32_e32 v6, v51, v209
	v_fmac_f32_e32 v7, v53, v209
	v_fmac_f32_e32 v9, v55, v209
	v_fmac_f32_e32 v10, v61, v209
	v_fmac_f32_e32 v11, v63, v209
	s_waitcnt lgkmcnt(0)
	ds_read_b64 v[42:43], v14 offset:456
	ds_read_b64 v[44:45], v14 offset:4552
	ds_read_b64 v[46:47], v14 offset:8648
	ds_read_b64 v[48:49], v14 offset:12744
	ds_read_b64 v[50:51], v14 offset:16840
	ds_read_b64 v[52:53], v14 offset:20936
	ds_read_b64 v[54:55], v14 offset:25032
	ds_read_b64 v[60:61], v14 offset:29128
	ds_read_b64 v[62:63], v14 offset:33224
	s_waitcnt vmcnt(12)
	v_fmac_f32_e32 v2, v24, v210
	v_fmac_f32_e32 v3, v26, v210
	v_fmac_f32_e32 v4, v28, v210
	v_fmac_f32_e32 v5, v30, v210
	v_fmac_f32_e32 v6, v32, v210
	v_fmac_f32_e32 v7, v34, v210
	v_fmac_f32_e32 v9, v36, v210
	v_fmac_f32_e32 v10, v38, v210
	v_fmac_f32_e32 v11, v40, v210
	v_fmac_f32_e32 v2, v25, v211
	v_fmac_f32_e32 v3, v27, v211
	v_fmac_f32_e32 v4, v29, v211
	v_fmac_f32_e32 v5, v31, v211
	v_fmac_f32_e32 v6, v33, v211
	v_fmac_f32_e32 v7, v35, v211
	v_fmac_f32_e32 v9, v37, v211
	v_fmac_f32_e32 v10, v39, v211
	v_fmac_f32_e32 v11, v41, v211
	s_waitcnt lgkmcnt(0)
	ds_read_b64 v[24:25], v14 offset:464
	ds_read_b64 v[26:27], v14 offset:4560
	ds_read_b64 v[28:29], v14 offset:8656
	ds_read_b64 v[30:31], v14 offset:12752
	ds_read_b64 v[32:33], v14 offset:16848
	ds_read_b64 v[34:35], v14 offset:20944
	ds_read_b64 v[36:37], v14 offset:25040
	ds_read_b64 v[38:39], v14 offset:29136
	ds_read_b64 v[40:41], v14 offset:33232
	v_fmac_f32_e32 v2, v42, v212
	v_fmac_f32_e32 v3, v44, v212
	v_fmac_f32_e32 v4, v46, v212
	v_fmac_f32_e32 v5, v48, v212
	v_fmac_f32_e32 v6, v50, v212
	v_fmac_f32_e32 v7, v52, v212
	v_fmac_f32_e32 v9, v54, v212
	v_fmac_f32_e32 v10, v60, v212
	v_fmac_f32_e32 v11, v62, v212
	v_fmac_f32_e32 v2, v43, v213
	v_fmac_f32_e32 v3, v45, v213
	v_fmac_f32_e32 v4, v47, v213
	v_fmac_f32_e32 v5, v49, v213
	v_fmac_f32_e32 v6, v51, v213
	v_fmac_f32_e32 v7, v53, v213
	v_fmac_f32_e32 v9, v55, v213
	v_fmac_f32_e32 v10, v61, v213
	v_fmac_f32_e32 v11, v63, v213
	s_waitcnt lgkmcnt(0)
	ds_read_b64 v[42:43], v14 offset:472
	ds_read_b64 v[44:45], v14 offset:4568
	ds_read_b64 v[46:47], v14 offset:8664
	ds_read_b64 v[48:49], v14 offset:12760
	ds_read_b64 v[50:51], v14 offset:16856
	ds_read_b64 v[52:53], v14 offset:20952
	ds_read_b64 v[54:55], v14 offset:25048
	ds_read_b64 v[60:61], v14 offset:29144
	ds_read_b64 v[62:63], v14 offset:33240
	s_waitcnt vmcnt(8)
	v_fmac_f32_e32 v2, v24, v214
	v_fmac_f32_e32 v3, v26, v214
	v_fmac_f32_e32 v4, v28, v214
	v_fmac_f32_e32 v5, v30, v214
	v_fmac_f32_e32 v6, v32, v214
	v_fmac_f32_e32 v7, v34, v214
	v_fmac_f32_e32 v9, v36, v214
	v_fmac_f32_e32 v10, v38, v214
	v_fmac_f32_e32 v11, v40, v214
	v_fmac_f32_e32 v2, v25, v215
	v_fmac_f32_e32 v3, v27, v215
	v_fmac_f32_e32 v4, v29, v215
	v_fmac_f32_e32 v5, v31, v215
	v_fmac_f32_e32 v6, v33, v215
	v_fmac_f32_e32 v7, v35, v215
	v_fmac_f32_e32 v9, v37, v215
	v_fmac_f32_e32 v10, v39, v215
	v_fmac_f32_e32 v11, v41, v215
	s_waitcnt lgkmcnt(0)
	ds_read_b64 v[24:25], v14 offset:480
	ds_read_b64 v[26:27], v14 offset:4576
	ds_read_b64 v[28:29], v14 offset:8672
	ds_read_b64 v[30:31], v14 offset:12768
	ds_read_b64 v[32:33], v14 offset:16864
	ds_read_b64 v[34:35], v14 offset:20960
	ds_read_b64 v[36:37], v14 offset:25056
	ds_read_b64 v[38:39], v14 offset:29152
	ds_read_b64 v[40:41], v14 offset:33248
	v_fmac_f32_e32 v2, v42, v216
	v_fmac_f32_e32 v3, v44, v216
	v_fmac_f32_e32 v4, v46, v216
	v_fmac_f32_e32 v5, v48, v216
	v_fmac_f32_e32 v6, v50, v216
	v_fmac_f32_e32 v7, v52, v216
	v_fmac_f32_e32 v9, v54, v216
	v_fmac_f32_e32 v10, v60, v216
	v_fmac_f32_e32 v11, v62, v216
	v_fmac_f32_e32 v2, v43, v217
	v_fmac_f32_e32 v3, v45, v217
	v_fmac_f32_e32 v4, v47, v217
	v_fmac_f32_e32 v5, v49, v217
	v_fmac_f32_e32 v6, v51, v217
	v_fmac_f32_e32 v7, v53, v217
	v_fmac_f32_e32 v9, v55, v217
	v_fmac_f32_e32 v10, v61, v217
	v_fmac_f32_e32 v11, v63, v217
	s_waitcnt lgkmcnt(0)
	ds_read_b64 v[42:43], v14 offset:488
	ds_read_b64 v[44:45], v14 offset:4584
	ds_read_b64 v[46:47], v14 offset:8680
	ds_read_b64 v[48:49], v14 offset:12776
	ds_read_b64 v[50:51], v14 offset:16872
	ds_read_b64 v[52:53], v14 offset:20968
	ds_read_b64 v[54:55], v14 offset:25064
	ds_read_b64 v[60:61], v14 offset:29160
	ds_read_b64 v[62:63], v14 offset:33256
	s_waitcnt vmcnt(4)
	v_fmac_f32_e32 v2, v24, v218
	v_fmac_f32_e32 v3, v26, v218
	v_fmac_f32_e32 v4, v28, v218
	v_fmac_f32_e32 v5, v30, v218
	v_fmac_f32_e32 v6, v32, v218
	v_fmac_f32_e32 v7, v34, v218
	v_fmac_f32_e32 v9, v36, v218
	v_fmac_f32_e32 v10, v38, v218
	v_fmac_f32_e32 v11, v40, v218
	v_fmac_f32_e32 v2, v25, v219
	v_fmac_f32_e32 v3, v27, v219
	v_fmac_f32_e32 v4, v29, v219
	v_fmac_f32_e32 v5, v31, v219
	v_fmac_f32_e32 v6, v33, v219
	v_fmac_f32_e32 v7, v35, v219
	v_fmac_f32_e32 v9, v37, v219
	v_fmac_f32_e32 v10, v39, v219
	v_fmac_f32_e32 v11, v41, v219
	s_waitcnt lgkmcnt(0)
	ds_read_b64 v[24:25], v14 offset:496
	ds_read_b64 v[26:27], v14 offset:4592
	ds_read_b64 v[28:29], v14 offset:8688
	ds_read_b64 v[30:31], v14 offset:12784
	ds_read_b64 v[32:33], v14 offset:16880
	ds_read_b64 v[34:35], v14 offset:20976
	ds_read_b64 v[36:37], v14 offset:25072
	ds_read_b64 v[38:39], v14 offset:29168
	ds_read_b64 v[40:41], v14 offset:33264
	v_fmac_f32_e32 v2, v42, v220
	v_fmac_f32_e32 v3, v44, v220
	v_fmac_f32_e32 v4, v46, v220
	v_fmac_f32_e32 v5, v48, v220
	v_fmac_f32_e32 v6, v50, v220
	v_fmac_f32_e32 v7, v52, v220
	v_fmac_f32_e32 v9, v54, v220
	v_fmac_f32_e32 v10, v60, v220
	v_fmac_f32_e32 v11, v62, v220
	v_fmac_f32_e32 v2, v43, v221
	v_fmac_f32_e32 v3, v45, v221
	v_fmac_f32_e32 v4, v47, v221
	v_fmac_f32_e32 v5, v49, v221
	v_fmac_f32_e32 v6, v51, v221
	v_fmac_f32_e32 v7, v53, v221
	v_fmac_f32_e32 v9, v55, v221
	v_fmac_f32_e32 v10, v61, v221
	v_fmac_f32_e32 v11, v63, v221
	s_waitcnt lgkmcnt(0)
	ds_read_b64 v[42:43], v14 offset:504
	ds_read_b64 v[44:45], v14 offset:4600
	ds_read_b64 v[46:47], v14 offset:8696
	ds_read_b64 v[48:49], v14 offset:12792
	ds_read_b64 v[50:51], v14 offset:16888
	ds_read_b64 v[52:53], v14 offset:20984
	ds_read_b64 v[54:55], v14 offset:25080
	ds_read_b64 v[60:61], v14 offset:29176
	ds_read_b64 v[62:63], v14 offset:33272
	s_waitcnt vmcnt(0)
	v_fmac_f32_e32 v2, v24, v222
	v_fmac_f32_e32 v3, v26, v222
	v_fmac_f32_e32 v4, v28, v222
	v_fmac_f32_e32 v5, v30, v222
	v_fmac_f32_e32 v6, v32, v222
	v_fmac_f32_e32 v7, v34, v222
	v_fmac_f32_e32 v9, v36, v222
	v_fmac_f32_e32 v10, v38, v222
	v_fmac_f32_e32 v11, v40, v222
	v_fmac_f32_e32 v2, v25, v223
	v_fmac_f32_e32 v3, v27, v223
	v_fmac_f32_e32 v4, v29, v223
	v_fmac_f32_e32 v5, v31, v223
	v_fmac_f32_e32 v6, v33, v223
	v_fmac_f32_e32 v7, v35, v223
	v_fmac_f32_e32 v9, v37, v223
	v_fmac_f32_e32 v10, v39, v223
	v_fmac_f32_e32 v11, v41, v223
	s_waitcnt lgkmcnt(0)
	v_fmac_f32_e32 v2, v42, v224
	v_fmac_f32_e32 v3, v44, v224
	v_fmac_f32_e32 v4, v46, v224
	v_fmac_f32_e32 v5, v48, v224
	v_fmac_f32_e32 v6, v50, v224
	v_fmac_f32_e32 v7, v52, v224
	v_fmac_f32_e32 v9, v54, v224
	v_fmac_f32_e32 v10, v60, v224
	v_fmac_f32_e32 v11, v62, v224
	v_fmac_f32_e32 v2, v43, v225
	v_fmac_f32_e32 v3, v45, v225
	v_fmac_f32_e32 v4, v47, v225
	v_fmac_f32_e32 v5, v49, v225
	v_fmac_f32_e32 v6, v51, v225
	v_fmac_f32_e32 v7, v53, v225
	v_fmac_f32_e32 v9, v55, v225
	v_fmac_f32_e32 v10, v61, v225
	v_fmac_f32_e32 v11, v63, v225
	s_mul_i32 s8, s43, 0x900
	s_add_i32 s8, s8, 0x1b000
	v_lshl_add_u32 v15, v22, 2, s8
	ds_write_b32 v15, v2
	ds_write_b32 v15, v3 offset:256
	ds_write_b32 v15, v4 offset:512
	ds_write_b32 v15, v5 offset:768
	ds_write_b32 v15, v6 offset:1024
	ds_write_b32 v15, v7 offset:1280
	ds_write_b32 v15, v9 offset:1536
	ds_write_b32 v15, v10 offset:1792
	ds_write_b32 v15, v11 offset:2048
	s_lshl_b32 s8, s43, 8
	s_add_i32 s8, s8, 0x1b000
	v_lshl_add_u32 v16, v22, 2, s8
	s_mul_i32 s8, s4, 0x36000
	s_mul_i32 s9, s43, 0x6000
	s_add_i32 s8, s8, s9
	s_add_i32 s8, s8, 0x100000
	s_add_u32 s8, s16, s8
	s_addc_u32 s9, s17, 0
	s_waitcnt lgkmcnt(0)
	s_barrier
	ds_read_b32 v24, v16
	ds_read_b32 v25, v16 offset:2304
	ds_read_b32 v26, v16 offset:4608
	ds_read_b32 v27, v16 offset:6912
	ds_read_b32 v28, v16 offset:9216
	ds_read_b32 v29, v16 offset:11520
	ds_read_b32 v30, v16 offset:13824
	ds_read_b32 v31, v16 offset:16128
	s_waitcnt lgkmcnt(6)
	v_add_f32_e32 v2, v24, v25
	s_waitcnt lgkmcnt(5)
	v_add_f32_e32 v2, v2, v26
	s_waitcnt lgkmcnt(4)
	v_add_f32_e32 v2, v2, v27
	s_waitcnt lgkmcnt(3)
	v_add_f32_e32 v2, v2, v28
	s_waitcnt lgkmcnt(2)
	v_add_f32_e32 v2, v2, v29
	s_waitcnt lgkmcnt(1)
	v_add_f32_e32 v2, v2, v30
	s_waitcnt lgkmcnt(0)
	v_add_f32_e32 v2, v2, v31
	v_add_f32_e32 v2, v2, v21
	global_store_dword v13, v2, s[8:9]
	s_cmp_lg_u32 s43, 0
	s_cbranch_scc1 .LBB0_23
	s_add_u32 s8, s8, 0x30000
	s_addc_u32 s9, s9, 0
	ds_read_b32 v24, v16 offset:2048
	ds_read_b32 v25, v16 offset:4352
	ds_read_b32 v26, v16 offset:6656
	ds_read_b32 v27, v16 offset:8960
	ds_read_b32 v28, v16 offset:11264
	ds_read_b32 v29, v16 offset:13568
	ds_read_b32 v30, v16 offset:15872
	ds_read_b32 v31, v16 offset:18176
	s_waitcnt lgkmcnt(6)
	v_add_f32_e32 v2, v24, v25
	s_waitcnt lgkmcnt(5)
	v_add_f32_e32 v2, v2, v26
	s_waitcnt lgkmcnt(4)
	v_add_f32_e32 v2, v2, v27
	s_waitcnt lgkmcnt(3)
	v_add_f32_e32 v2, v2, v28
	s_waitcnt lgkmcnt(2)
	v_add_f32_e32 v2, v2, v29
	s_waitcnt lgkmcnt(1)
	v_add_f32_e32 v2, v2, v30
	s_waitcnt lgkmcnt(0)
	v_add_f32_e32 v2, v2, v31
	v_add_f32_e32 v2, v2, v21
	global_store_dword v13, v2, s[8:9]

.LBB0_180:
	s_cmp_lt_i32 s90, 2
	s_cselect_b64 s[0:1], -1, 0
	s_and_b64 s[4:5], s[0:1], s[4:5]
	s_andn2_b64 vcc, exec, s[4:5]
	s_cbranch_vccnz .LBB0_220
	s_cmp_lt_i32 s82, 32
	s_cselect_b64 s[16:17], -1, 0
	s_ashr_i32 s64, s82, 1
	s_lshl_b32 s4, s64, 18
	s_and_b32 s8, s4, 0xc0000
	s_lshl_b32 s4, s64, 6
	s_mov_b64 s[6:7], s[84:85]
	s_and_b32 s65, s82, 1
	s_and_b32 s9, s4, 0xffffff00
	s_load_dwordx2 s[4:5], s[6:7], 0x100
	s_lshl_b32 s10, s65, 17
	s_ashr_i32 s11, s9, 31
	s_add_u32 s8, s8, s9
	s_addc_u32 s9, 0, s11
	s_lshl_b64 s[14:15], s[8:9], 1
	s_waitcnt lgkmcnt(0)
	s_add_u32 s62, s4, 0x198000
	s_addc_u32 s63, s5, 0
	s_add_u32 s8, s62, s10
	s_addc_u32 s9, s63, 0
	s_add_u32 s12, s8, 0x10000
	s_addc_u32 s13, s9, 0
	s_mov_b32 s18, s86
	v_mbcnt_hi_u32_b32 v1, -1, v132
	s_add_u32 s10, s8, 0x80
	s_addc_u32 s11, s9, 0
	v_lshl_add_u32 v2, s18, 6, v1
	s_and_b64 vcc, exec, s[16:17]
	v_readfirstlane_b32 s24, v2
	s_mov_b32 s8, s86
	s_nop 0
	v_lshl_add_u32 v3, s8, 6, v1
	s_movk_i32 s8, 0x4200
	v_ashrrev_i32_e32 v2, 6, v3
	v_lshl_add_u32 v1, s82, 3, v2
	v_cmp_gt_i32_e32 vcc, s8, v1
	s_and_saveexec_b64 s[8:9], vcc
	s_xor_b64 s[8:9], exec, s[8:9]
	s_cbranch_execz .LBB0_219
	v_and_b32_e32 v3, 63, v3
	v_lshlrev_b32_e32 v98, 2, v3
	v_mov_b32_e32 v99, 0
	s_load_dwordx2 s[14:15], s[6:7], 0x0
	s_load_dwordx2 s[16:17], s[6:7], 0x10
	v_lshl_add_u64 v[4:5], s[4:5], 0, v[98:99]
	s_mov_b64 s[6:7], 0x7bc00000
	v_lshl_add_u64 v[100:101], v[4:5], 0, s[6:7]
	v_lshlrev_b32_e32 v4, 4, v3
	v_mov_b32_e32 v5, v99
	v_lshl_add_u64 v[4:5], s[4:5], 0, v[4:5]
	s_mov_b64 s[6:7], 0x100000
	v_lshl_add_u64 v[102:103], v[4:5], 0, s[6:7]
	v_lshlrev_b32_e32 v4, 3, v3
	v_mov_b32_e32 v5, v99
	v_lshlrev_b32_e32 v2, 2, v2
	v_lshl_add_u64 v[4:5], s[4:5], 0, v[4:5]
	s_mov_b64 s[4:5], 0x12900000
	v_lshl_add_u32 v2, s82, 5, v2
	s_lshl_b32 s10, s83, 3
	v_lshl_add_u64 v[104:105], v[4:5], 0, s[4:5]
	v_or_b32_e32 v106, 3, v2
	s_lshl_b32 s11, s83, 5
	v_mov_b32_e32 v118, -1
	s_mov_b64 s[4:5], 0
	s_movk_i32 s12, 0x4000
	s_waitcnt lgkmcnt(0)
	v_mov_b32_e32 v114, s17
	v_mov_b32_e32 v115, s15
	v_mov_b32_e32 v116, s16
	v_mov_b32_e32 v117, s14
	v_lshlrev_b32_e32 v98, 2, v98
	s_mov_b32 s13, 0x10000
	s_movk_i32 s14, 0x41ff
	s_branch .LBB0_216

.LBB0_219:
	s_or_b64 exec, exec, s[8:9]
	s_cmp_lt_i32 s82, 32
	s_cselect_b64 s[16:17], -1, 0
	s_ashr_i32 s64, s82, 1
	s_lshl_b32 s4, s64, 18
	s_and_b32 s8, s4, 0xc0000
	s_lshl_b32 s4, s64, 6
	s_mov_b64 s[6:7], s[84:85]
	s_and_b32 s65, s82, 1
	s_and_b32 s9, s4, 0xffffff00
	s_load_dwordx2 s[4:5], s[6:7], 0x100
	s_lshl_b32 s10, s65, 17
	s_ashr_i32 s11, s9, 31
	s_add_u32 s8, s8, s9
	s_addc_u32 s9, 0, s11
	s_lshl_b64 s[14:15], s[8:9], 1
	s_waitcnt lgkmcnt(0)
	s_add_u32 s62, s4, 0x198000
	s_addc_u32 s63, s5, 0
	s_add_u32 s8, s62, s10
	s_addc_u32 s9, s63, 0
	s_add_u32 s12, s8, 0x10000
	s_addc_u32 s13, s9, 0
	s_mov_b32 s18, s86
	v_mbcnt_hi_u32_b32 v1, -1, v132
	s_add_u32 s10, s8, 0x80
	s_addc_u32 s11, s9, 0
	v_lshl_add_u32 v2, s18, 6, v1
	s_and_b64 vcc, exec, s[16:17]
	v_readfirstlane_b32 s24, v2
	s_cbranch_vccz .LBB0_197
	v_bfe_i32 v5, v2, 27, 1
	v_lshlrev_b32_e32 v3, 4, v2
	v_lshrrev_b32_e32 v5, 22, v5
	v_add_u32_e32 v5, v3, v5
	v_and_b32_e32 v5, 0xfffffc00, v5
	v_sub_u32_e32 v5, v3, v5
	v_ashrrev_i32_e32 v4, 31, v2
	v_lshrrev_b32_e32 v6, 4, v5
	v_lshrrev_b32_e32 v4, 26, v4
	v_bitop3_b32 v6, v6, v5, 32 bitop3:0x6c
	v_ashrrev_i32_e32 v5, 31, v5
	v_add_u32_e32 v4, v2, v4
	v_lshrrev_b32_e32 v5, 26, v5
	v_ashrrev_i32_e32 v4, 6, v4
	v_add_u32_e32 v5, v6, v5
	v_lshlrev_b32_e32 v7, 3, v4
	v_ashrrev_i32_e32 v5, 6, v5
	v_and_b32_e32 v7, -16, v7
	v_mul_i32_i24_e32 v8, 64, v5
	v_add_u32_e32 v7, v5, v7
	v_sub_u32_e32 v6, v6, v8
	v_mov_b32_e32 v8, 1
	v_lshlrev_b32_e32 v4, 5, v4
	v_ashrrev_i16_sdwa v6, v8, sext(v6) dst_sel:DWORD dst_unused:UNUSED_PAD src0_sel:DWORD src1_sel:BYTE_0
	v_lshlrev_b32_e32 v9, 1, v7
	v_lshrrev_b32_e32 v10, 2, v7
	v_and_b32_e32 v5, 3, v5
	s_mov_b32 s18, 0x1fffe0
	v_and_b32_e32 v4, 32, v4
	v_bfe_i32 v6, v6, 0, 16
	v_and_b32_e32 v9, 24, v9
	v_and_b32_e32 v10, 4, v10
	v_and_or_b32 v5, v7, s18, v5
	v_or3_b32 v5, v5, v10, v9
	v_add_lshl_u32 v4, v4, v6, 1
	v_add_u32_e32 v3, 0x2000, v3
	v_lshl_add_u32 v133, v7, 9, v4
	v_lshl_add_u32 v134, v5, 11, v4
	v_ashrrev_i32_e32 v4, 31, v3
	v_lshrrev_b32_e32 v4, 22, v4
	v_add_u32_e32 v4, v3, v4
	v_ashrrev_i32_e32 v4, 10, v4
	v_mul_i32_i24_e32 v5, 0x400, v4
	v_sub_u32_e32 v3, v3, v5
	v_lshrrev_b32_e32 v5, 4, v3
	v_bitop3_b32 v3, v5, v3, 32 bitop3:0x6c
	v_ashrrev_i32_e32 v6, 31, v3
	v_lshrrev_b32_e32 v6, 26, v6
	s_add_u32 s66, s4, 0x3400000
	v_lshlrev_b32_e32 v5, 3, v4
	v_add_u32_e32 v6, v3, v6
	s_addc_u32 s67, s5, 0
	v_and_b32_e32 v5, -16, v5
	v_ashrrev_i32_e32 v7, 6, v6
	v_and_b32_e32 v6, 0xc0, v6
	s_ashr_i32 s37, s24, 6
	s_ashr_i32 s25, s24, 8
	v_add_u32_e32 v5, v7, v5
	v_sub_u32_e32 v3, v3, v6
	s_lshl_b32 s27, s37, 10
	v_lshlrev_b32_e32 v4, 5, v4
	v_ashrrev_i16_sdwa v3, v8, sext(v3) dst_sel:DWORD dst_unused:UNUSED_PAD src0_sel:DWORD src1_sel:BYTE_0
	v_lshlrev_b32_e32 v6, 1, v5
	v_lshrrev_b32_e32 v8, 2, v5
	v_and_b32_e32 v7, 3, v7
	s_add_u32 s40, s66, s14
	v_and_b32_e32 v4, 32, v4
	v_bfe_i32 v3, v3, 0, 16
	v_and_b32_e32 v6, 24, v6
	v_and_b32_e32 v8, 4, v8
	v_and_or_b32 v7, v5, s18, v7
	s_addc_u32 s41, s67, s15
	s_add_i32 s26, s27, 0
	v_or3_b32 v6, v7, v8, v6
	v_add_lshl_u32 v3, v4, v3, 1
	s_add_i32 s28, s26, 0x10000
	s_mov_b32 s18, m0
	s_mov_b32 m0, s28
	s_nop 3
	global_load_lds_dwordx4 v134, s[40:41]
	s_mov_b32 m0, s18
	s_add_i32 s29, s26, 0x12000
	v_lshl_add_u32 v136, v6, 11, v3
	s_mov_b32 s18, m0
	s_mov_b32 m0, s29
	s_nop 3
	global_load_lds_dwordx4 v136, s[40:41]
	s_mov_b32 m0, s18
	s_add_u32 s20, s40, 0x40000
	s_addc_u32 s21, s41, 0
	s_add_i32 s30, s26, 0x14000
	s_mov_b32 s22, m0
	s_mov_b32 m0, s30
	s_nop 3
	global_load_lds_dwordx4 v134, s[20:21]
	s_mov_b32 m0, s22
	s_add_i32 s31, s26, 0x16000
	s_mov_b32 s22, m0
	s_mov_b32 m0, s31
	s_nop 3
	global_load_lds_dwordx4 v136, s[20:21]
	s_mov_b32 m0, s22
	s_mov_b32 s20, m0
	s_mov_b32 m0, s26
	s_nop 3
	global_load_lds_dwordx4 v133, s[8:9]
	s_mov_b32 m0, s20
	v_lshl_add_u32 v135, v5, 9, v3
	s_add_i32 s34, s26, 0x2000
	s_mov_b32 s20, m0
	s_mov_b32 m0, s34
	s_nop 3
	global_load_lds_dwordx4 v135, s[8:9]
	s_mov_b32 m0, s20
	s_add_i32 s35, s26, 0x4000
	s_mov_b32 s20, m0
	s_mov_b32 m0, s35
	s_nop 3
	global_load_lds_dwordx4 v133, s[12:13]
	s_mov_b32 m0, s20
	s_add_i32 s36, s26, 0x6000
	s_mov_b32 s22, m0
	s_mov_b32 m0, s36
	s_nop 3
	global_load_lds_dwordx4 v135, s[12:13]
	s_mov_b32 m0, s22
	s_cmp_eq_u32 s25, 1
	s_mov_b64 s[18:19], 0x40000
	s_cselect_b64 s[20:21], -1, 0
	s_cmp_lg_u32 s25, 1
	s_cbranch_scc1 .LBB0_184
	s_barrier

.LBB0_213:
.LBB0_220:
	s_cmp_gt_i32 s91, 2
	s_cselect_b64 s[4:5], -1, 0
	s_and_b64 s[0:1], s[0:1], s[4:5]
	s_andn2_b64 vcc, exec, s[0:1]
	s_cbranch_vccnz .LBB0_270
	s_waitcnt vmcnt(0)
	v_cmp_eq_u32_e32 vcc, 0, v0
	s_barrier
	s_and_saveexec_b64 s[0:1], vcc
	s_cbranch_execz .LBB0_269
	v_readlane_b32 s4, v251, 2
	s_waitcnt vmcnt(0) expcnt(0) lgkmcnt(0)
	s_nop 0
	v_mov_b32_e32 v1, s4
	ds_read_b32 v3, v1
	ds_read_b32 v1, v1 offset:4
	s_waitcnt lgkmcnt(1)
	v_cmp_ne_u32_e32 vcc, 0, v3
	s_cbranch_vccnz .LBB0_237
	v_readlane_b32 s4, v251, 0
	v_readlane_b32 s5, v251, 1
	s_load_dwordx2 s[8:9], s[4:5], 0x4
	s_add_u32 s4, s88, 0x4200
	s_addc_u32 s5, s89, 0
	s_add_u32 s6, s88, 0x4400
	s_addc_u32 s7, s89, 0
	s_waitcnt lgkmcnt(0)
	s_mul_i32 s46, s8, s83
	s_add_u32 s8, s88, 0x4500
	s_mul_i32 s46, s46, s9
	s_addc_u32 s9, s89, 0
	s_add_u32 s10, s88, 0x4600
	s_addc_u32 s11, s89, 0
	s_add_u32 s12, s88, 0x4700
	s_addc_u32 s13, s89, 0
	s_add_u32 s14, s88, 0x4800
	s_addc_u32 s15, s89, 0
	s_add_u32 s16, s88, 0x4900
	s_addc_u32 s17, s89, 0
	s_add_u32 s18, s88, 0x4a00
	s_addc_u32 s19, s89, 0
	s_add_u32 s20, s88, 0x4b00
	s_addc_u32 s21, s89, 0
	s_add_u32 s22, s88, 0x4c00
	s_addc_u32 s23, s89, 0
	s_add_u32 s24, s88, 0x4d00
	s_addc_u32 s25, s89, 0
	s_add_u32 s26, s88, 0x4e00
	s_addc_u32 s27, s89, 0
	s_add_u32 s28, s88, 0x4f00
	s_addc_u32 s29, s89, 0
	s_add_u32 s30, s88, 0x5000
	s_addc_u32 s31, s89, 0
	s_add_u32 s34, s88, 0x5100
	s_addc_u32 s35, s89, 0
	s_add_u32 s36, s88, 0x5200
	s_addc_u32 s37, s89, 0
	s_add_u32 s38, s88, 0x5300
	s_addc_u32 s39, s89, 0
	s_mov_b32 s47, 1
	v_mov_b32_e32 v17, 0
	s_branch .LBB0_225
